# dense loop variant 4: P.V of tile n-2, exp/sum/pack of tile n-1 and QK of tile n in one region (two score buffers, V fragments prefetched before the barrier)
# speedup vs baseline: 1.0093x; 1.0004x over previous
.LBB0_408:
	s_lshr_b32 s4, s72, 3
	s_lshl_b32 s5, s72, 5
	s_bfe_u32 s10, s72, 0x20001
	s_ashr_i32 s9, s72, 8
	s_and_b32 s4, s4, 16
	s_and_b32 s11, s5, 32
	s_lshl_b32 s8, s10, 7
	s_or_b32 s4, s11, s4
	s_lshl_b32 s13, s9, 12
	s_mul_i32 s11, s9, 0x5c00000
	s_mul_hi_i32 s12, s13, 0x5c00
	s_add_u32 s11, s18, s11
	s_addc_u32 s12, s19, s12
	s_and_b32 s14, s5, 0xf00
	s_mul_i32 s5, s14, 0x5c00
	s_add_u32 s5, s11, s5
	s_addc_u32 s11, s12, 0
	s_lshl_b32 s12, s10, 9
	s_lshl_b32 s4, s4, 3
	s_or_b32 s12, s4, s12
	s_lshl_b32 s4, s12, 1
	s_add_u32 s4, s5, s4
	s_addc_u32 s5, s11, 0
	v_mov_b32_e32 v147, v3
	v_lshl_add_u64 v[8:9], s[4:5], 0, v[146:147]
	v_add_co_u32_e32 v4, vcc, s54, v8
	v_lshl_add_u64 v[32:33], v[8:9], 0, s[24:25]
	s_nop 0
	v_addc_co_u32_e32 v5, vcc, 0, v9, vcc
	global_load_dwordx4 v[4:7], v[4:5], off offset:1024
	s_nop 0
	global_load_dwordx4 v[8:11], v[32:33], off offset:16
	global_load_dwordx4 v[12:15], v[32:33], off offset:32
	global_load_dwordx4 v[16:19], v[32:33], off offset:48
	global_load_dwordx4 v[20:23], v[32:33], off offset:128
	global_load_dwordx4 v[24:27], v[32:33], off offset:160
	global_load_dwordx4 v[28:31], v[32:33], off offset:144
	s_lshl_b32 s4, s9, 2
	s_or_b32 s10, s4, s10
	s_lshl_b32 s4, s10, 12
	s_ashr_i32 s5, s4, 31
	global_load_dwordx4 v[32:35], v[32:33], off offset:176
	s_lshl_b64 s[4:5], s[4:5], 7
	s_add_u32 s4, s49, s4
	s_addc_u32 s5, s50, s5
	s_lshl_b32 s10, s10, 7
	s_ashr_i32 s11, s10, 31
	v_lshl_add_u64 v[36:37], s[4:5], 0, v[138:139]
	s_lshl_b64 s[10:11], s[10:11], 12
	v_lshl_add_u64 v[38:39], v[36:37], 0, v[136:137]
	v_lshl_add_u64 v[36:37], v[140:141], 0, s[10:11]
	global_load_dwordx4 v[40:43], v[36:37], off
	global_load_dwordx4 v[44:47], v[38:39], off
	v_mov_b32_e32 v106, v3
	v_mov_b32_e32 v100, v3
	v_mov_b32_e32 v101, v3
	v_mov_b32_e32 v107, v3
	v_mov_b32_e32 v108, v3
	v_mov_b32_e32 v109, v3
	v_mov_b32_e32 v110, v3
	v_mov_b32_e32 v111, v3
	v_mov_b32_e32 v112, v3
	v_mov_b32_e32 v113, v3
	v_mov_b32_e32 v114, v3
	v_mov_b32_e32 v102, v3
	v_mov_b32_e32 v103, v3
	v_mov_b32_e32 v104, v3
	v_mov_b32_e32 v105, v3
	s_waitcnt vmcnt(0)
	v_mov_b32_e32 v115, v3
	v_lshl_add_u64 v[148:149], s[4:5], 0, v[136:137]
	s_mov_b32 s15, 1
	v_mov_b32_e32 v145, 0
	v_mov_b32_e32 v152, v186
	s_waitcnt vmcnt(8)
	v_lshlrev_b32_e32 v51, 16, v8
	v_and_b32_e32 v8, 0xffff0000, v8
	s_waitcnt vmcnt(6)
	v_lshlrev_b32_e32 v59, 16, v16
	v_and_b32_e32 v16, 0xffff0000, v16
	v_lshlrev_b32_e32 v2, 16, v4
	v_and_b32_e32 v4, 0xffff0000, v4
	v_mul_f32_e32 v59, 0x3f8293ee, v59
	v_mul_f32_e32 v16, 0x3f8293ee, v16
	v_cvt_pk_fp8_f32 v106, v59, v16
	v_mul_f32_e32 v2, 0x3f8293ee, v2
	v_mul_f32_e32 v4, 0x3f8293ee, v4
	v_cvt_pk_fp8_f32 v100, v2, v4
	v_lshlrev_b32_e32 v60, 16, v17
	v_and_b32_e32 v2, 0xffff0000, v17
	v_lshlrev_b32_e32 v48, 16, v5
	v_and_b32_e32 v5, 0xffff0000, v5
	v_lshlrev_b32_e32 v49, 16, v6
	v_and_b32_e32 v6, 0xffff0000, v6
	v_mul_f32_e32 v60, 0x3f8293ee, v60
	v_mul_f32_e32 v2, 0x3f8293ee, v2
	v_cvt_pk_fp8_f32 v106, v60, v2 op_sel:[0,0,1]
	v_lshlrev_b32_e32 v2, 16, v18
	v_and_b32_e32 v4, 0xffff0000, v18
	v_mul_f32_e32 v49, 0x3f8293ee, v49
	v_mul_f32_e32 v6, 0x3f8293ee, v6
	v_cvt_pk_fp8_f32 v101, v49, v6
	v_mul_f32_e32 v48, 0x3f8293ee, v48
	v_mul_f32_e32 v5, 0x3f8293ee, v5
	v_cvt_pk_fp8_f32 v100, v48, v5 op_sel:[0,0,1]
	v_mul_f32_e32 v2, 0x3f8293ee, v2
	v_mul_f32_e32 v4, 0x3f8293ee, v4
	v_cvt_pk_fp8_f32 v107, v2, v4
	s_waitcnt vmcnt(5)
	v_lshlrev_b32_e32 v5, 16, v20
	v_and_b32_e32 v6, 0xffff0000, v20
	v_mul_f32_e32 v5, 0x3f8293ee, v5
	v_mul_f32_e32 v6, 0x3f8293ee, v6
	v_cvt_pk_fp8_f32 v108, v5, v6
	v_lshlrev_b32_e32 v2, 16, v19
	v_and_b32_e32 v4, 0xffff0000, v19
	v_mul_f32_e32 v2, 0x3f8293ee, v2
	v_mul_f32_e32 v4, 0x3f8293ee, v4
	v_cvt_pk_fp8_f32 v107, v2, v4 op_sel:[0,0,1]
	v_lshlrev_b32_e32 v2, 16, v21
	v_and_b32_e32 v4, 0xffff0000, v21
	v_mul_f32_e32 v2, 0x3f8293ee, v2
	v_mul_f32_e32 v4, 0x3f8293ee, v4
	v_cvt_pk_fp8_f32 v108, v2, v4 op_sel:[0,0,1]
	v_lshlrev_b32_e32 v2, 16, v22
	v_and_b32_e32 v4, 0xffff0000, v22
	v_mul_f32_e32 v2, 0x3f8293ee, v2
	v_mul_f32_e32 v4, 0x3f8293ee, v4
	v_cvt_pk_fp8_f32 v109, v2, v4
	s_waitcnt vmcnt(3)
	v_lshlrev_b32_e32 v5, 16, v28
	v_and_b32_e32 v6, 0xffff0000, v28
	v_mul_f32_e32 v5, 0x3f8293ee, v5
	v_mul_f32_e32 v6, 0x3f8293ee, v6
	v_cvt_pk_fp8_f32 v110, v5, v6
	v_lshlrev_b32_e32 v2, 16, v23
	v_and_b32_e32 v4, 0xffff0000, v23
	v_mul_f32_e32 v2, 0x3f8293ee, v2
	v_mul_f32_e32 v4, 0x3f8293ee, v4
	v_cvt_pk_fp8_f32 v109, v2, v4 op_sel:[0,0,1]
	v_lshlrev_b32_e32 v2, 16, v29
	v_and_b32_e32 v4, 0xffff0000, v29
	v_mul_f32_e32 v2, 0x3f8293ee, v2
	v_mul_f32_e32 v4, 0x3f8293ee, v4
	v_cvt_pk_fp8_f32 v110, v2, v4 op_sel:[0,0,1]
	v_lshlrev_b32_e32 v2, 16, v30
	v_and_b32_e32 v4, 0xffff0000, v30
	v_mul_f32_e32 v2, 0x3f8293ee, v2
	v_mul_f32_e32 v4, 0x3f8293ee, v4
	v_cvt_pk_fp8_f32 v111, v2, v4
	v_lshlrev_b32_e32 v5, 16, v24
	v_and_b32_e32 v6, 0xffff0000, v24
	v_mul_f32_e32 v5, 0x3f8293ee, v5
	v_mul_f32_e32 v6, 0x3f8293ee, v6
	v_cvt_pk_fp8_f32 v112, v5, v6
	v_lshlrev_b32_e32 v2, 16, v31
	v_and_b32_e32 v4, 0xffff0000, v31
	v_mul_f32_e32 v2, 0x3f8293ee, v2
	v_mul_f32_e32 v4, 0x3f8293ee, v4
	v_cvt_pk_fp8_f32 v111, v2, v4 op_sel:[0,0,1]
	v_lshlrev_b32_e32 v2, 16, v25
	v_and_b32_e32 v4, 0xffff0000, v25
	v_mul_f32_e32 v2, 0x3f8293ee, v2
	v_mul_f32_e32 v4, 0x3f8293ee, v4
	v_cvt_pk_fp8_f32 v112, v2, v4 op_sel:[0,0,1]
	v_lshlrev_b32_e32 v2, 16, v26
	v_and_b32_e32 v4, 0xffff0000, v26
	v_mul_f32_e32 v2, 0x3f8293ee, v2
	v_mul_f32_e32 v4, 0x3f8293ee, v4
	v_cvt_pk_fp8_f32 v113, v2, v4
	s_waitcnt vmcnt(2)
	v_lshlrev_b32_e32 v5, 16, v32
	v_and_b32_e32 v6, 0xffff0000, v32
	v_lshlrev_b32_e32 v53, 16, v10
	v_and_b32_e32 v10, 0xffff0000, v10
	v_mul_f32_e32 v5, 0x3f8293ee, v5
	v_mul_f32_e32 v6, 0x3f8293ee, v6
	v_cvt_pk_fp8_f32 v114, v5, v6
	v_mul_f32_e32 v51, 0x3f8293ee, v51
	v_mul_f32_e32 v8, 0x3f8293ee, v8
	v_cvt_pk_fp8_f32 v102, v51, v8
	v_mul_f32_e32 v53, 0x3f8293ee, v53
	v_mul_f32_e32 v10, 0x3f8293ee, v10
	v_cvt_pk_fp8_f32 v103, v53, v10
	v_lshlrev_b32_e32 v2, 16, v27
	v_and_b32_e32 v4, 0xffff0000, v27
	v_mul_f32_e32 v2, 0x3f8293ee, v2
	v_mul_f32_e32 v4, 0x3f8293ee, v4
	v_cvt_pk_fp8_f32 v113, v2, v4 op_sel:[0,0,1]
	v_lshlrev_b32_e32 v2, 16, v33
	v_and_b32_e32 v4, 0xffff0000, v33
	v_lshlrev_b32_e32 v50, 16, v7
	v_and_b32_e32 v7, 0xffff0000, v7
	v_lshlrev_b32_e32 v52, 16, v9
	v_and_b32_e32 v9, 0xffff0000, v9
	v_lshlrev_b32_e32 v54, 16, v11
	v_and_b32_e32 v11, 0xffff0000, v11
	v_mul_f32_e32 v2, 0x3f8293ee, v2
	v_mul_f32_e32 v4, 0x3f8293ee, v4
	v_cvt_pk_fp8_f32 v114, v2, v4 op_sel:[0,0,1]
	s_waitcnt vmcnt(1)
	v_mov_b32_e32 v4, v40
	v_mov_b32_e32 v5, v42
	v_mov_b32_e32 v42, v41
	v_lshlrev_b32_e32 v55, 16, v12
	v_and_b32_e32 v12, 0xffff0000, v12
	v_lshlrev_b32_e32 v57, 16, v14
	v_and_b32_e32 v14, 0xffff0000, v14
	v_mul_f32_e32 v50, 0x3f8293ee, v50
	v_mul_f32_e32 v7, 0x3f8293ee, v7
	v_cvt_pk_fp8_f32 v101, v50, v7 op_sel:[0,0,1]
	v_mul_f32_e32 v52, 0x3f8293ee, v52
	v_mul_f32_e32 v9, 0x3f8293ee, v9
	v_cvt_pk_fp8_f32 v102, v52, v9 op_sel:[0,0,1]
	v_mul_f32_e32 v54, 0x3f8293ee, v54
	v_mul_f32_e32 v11, 0x3f8293ee, v11
	v_cvt_pk_fp8_f32 v103, v54, v11 op_sel:[0,0,1]
	ds_write_b64 v189, v[4:5]
	ds_write_b64 v190, v[42:43]
	s_waitcnt vmcnt(0)
	ds_write_b128 v191, v[44:47] offset:32768
	s_waitcnt lgkmcnt(0)
	s_barrier
	ds_read_b128 v[40:43], v192 offset:36864
	ds_read_b128 v[4:7], v192 offset:32768
	ds_read_b128 v[44:47], v193 offset:36864
	ds_read_b128 v[8:11], v193 offset:32768
	v_mul_f32_e32 v55, 0x3f8293ee, v55
	v_mul_f32_e32 v12, 0x3f8293ee, v12
	v_cvt_pk_fp8_f32 v104, v55, v12
	v_mul_f32_e32 v57, 0x3f8293ee, v57
	v_mul_f32_e32 v14, 0x3f8293ee, v14
	v_cvt_pk_fp8_f32 v105, v57, v14
	v_lshlrev_b32_e32 v56, 16, v13
	v_and_b32_e32 v13, 0xffff0000, v13
	v_lshlrev_b32_e32 v58, 16, v15
	v_and_b32_e32 v15, 0xffff0000, v15
	v_lshlrev_b32_e32 v2, 16, v34
	v_and_b32_e32 v12, 0xffff0000, v34
	v_mul_f32_e32 v56, 0x3f8293ee, v56
	v_mul_f32_e32 v13, 0x3f8293ee, v13
	v_cvt_pk_fp8_f32 v104, v56, v13 op_sel:[0,0,1]
	v_mul_f32_e32 v58, 0x3f8293ee, v58
	v_mul_f32_e32 v15, 0x3f8293ee, v15
	v_cvt_pk_fp8_f32 v105, v58, v15 op_sel:[0,0,1]
	v_mul_f32_e32 v2, 0x3f8293ee, v2
	v_mul_f32_e32 v12, 0x3f8293ee, v12
	v_cvt_pk_fp8_f32 v115, v2, v12
	v_lshlrev_b32_e32 v2, 16, v35
	v_and_b32_e32 v56, 0xffff0000, v35
	s_waitcnt lgkmcnt(0)
	v_mfma_scale_f32_32x32x64_f8f6f4 v[20:35], v[4:11], v[100:107], 0, v188, v188 op_sel_hi:[0,0,0]
	v_mfma_scale_f32_32x32x64_f8f6f4 v[4:19], v[40:47], v[100:107], 0, v188, v188 op_sel_hi:[0,0,0]
	ds_read_b128 v[40:43], v194 offset:36864
	ds_read_b128 v[48:51], v194 offset:32768
	ds_read_b128 v[44:47], v195 offset:36864
	ds_read_b128 v[52:55], v195 offset:32768
	v_mul_f32_e32 v2, 0x3f8293ee, v2
	v_mul_f32_e32 v56, 0x3f8293ee, v56
	v_cvt_pk_fp8_f32 v115, v2, v56 op_sel:[0,0,1]
	s_waitcnt lgkmcnt(0)
	v_mfma_scale_f32_32x32x64_f8f6f4 v[20:35], v[48:55], v[108:115], v[20:35], v188, v188 op_sel_hi:[0,0,0]
	v_mfma_scale_f32_32x32x64_f8f6f4 v[4:19], v[40:47], v[108:115], v[4:19], v188, v188 op_sel_hi:[0,0,0]
	v_add_co_u32_e32 v44, vcc, s56, v38
	s_nop 15
	s_nop 15
	s_nop 0
	v_max_f32_e32 v2, v21, v21
	v_max_f32_e32 v40, v20, v20
	v_max_f32_e32 v2, v40, v2
	v_max3_f32 v2, v2, v22, v23
	v_max3_f32 v2, v2, v24, v25
	v_max3_f32 v2, v2, v26, v27
	v_max3_f32 v2, v2, v28, v29
	v_max3_f32 v2, v2, v30, v31
	v_max3_f32 v2, v2, v32, v33
	v_max3_f32 v2, v2, v34, v35
	v_max3_f32 v2, v2, v4, v5
	v_max3_f32 v2, v2, v6, v7
	v_max3_f32 v2, v2, v8, v9
	v_max3_f32 v2, v2, v10, v11
	v_max3_f32 v2, v2, v12, v13
	v_max3_f32 v2, v2, v14, v15
	v_max3_f32 v2, v2, v16, v17
	v_max3_f32 v2, v2, v18, v19
	v_mov_b32_e32 v48, v2
	s_nop 1
	v_permlane32_swap_b32_e32 v2, v48
	v_max_f32_e32 v48, v48, v48
	v_max_f32_e32 v2, v2, v2
	v_max_f32_e32 v2, v2, v48
	v_addc_co_u32_e32 v45, vcc, 0, v39, vcc
	v_add_f32_e32 v48, 0x7149f2ca, v2
	v_max_f32_e32 v2, 0xf149f2ca, v2
	v_cmp_ge_f32_e32 vcc, s55, v48
	v_sub_f32_e32 v48, 0xf149f2ca, v2
	v_mul_f32_e32 v48, 0x3e000000, v48
	v_exp_f32_e32 v48, v48
	global_load_dwordx4 v[40:43], v[36:37], off offset:64
	s_cmp_eq_u64 vcc, exec
	s_cselect_b64 vcc, -1, 0
	global_load_dwordx4 v[44:47], v[44:45], off
	v_cndmask_b32_e32 v153, v2, v196, vcc
	v_cndmask_b32_e64 v147, v48, 1.0, vcc
	v_add_co_u32_e32 v38, vcc, s52, v38
	v_mul_f32_e32 v2, 0xbe000000, v153
	s_nop 0
	v_addc_co_u32_e32 v39, vcc, 0, v39, vcc
	global_load_dwordx4 v[120:123], v[38:39], off
	global_load_dwordx4 v[116:119], v[36:37], off offset:128
	v_mov_b32_e32 v36, v2
	v_fmamk_f32 v20, v20, 0x3e000000, v2
	v_fmamk_f32 v21, v21, 0x3e000000, v2
	v_fmamk_f32 v22, v22, 0x3e000000, v2
	v_fmamk_f32 v23, v23, 0x3e000000, v2
	v_fmamk_f32 v24, v24, 0x3e000000, v2
	v_fmamk_f32 v25, v25, 0x3e000000, v2
	v_fmamk_f32 v26, v26, 0x3e000000, v2
	v_fmamk_f32 v27, v27, 0x3e000000, v2
	v_fmamk_f32 v28, v28, 0x3e000000, v2
	v_fmamk_f32 v29, v29, 0x3e000000, v2
	v_fmamk_f32 v30, v30, 0x3e000000, v2
	v_fmamk_f32 v31, v31, 0x3e000000, v2
	v_fmamk_f32 v32, v32, 0x3e000000, v2
	v_fmamk_f32 v33, v33, 0x3e000000, v2
	v_fmamk_f32 v34, v34, 0x3e000000, v2
	v_fmac_f32_e32 v36, 0x3e000000, v35
	s_lshl_b32 s4, s9, 9
	v_pk_fma_f32 v[158:159], v[16:17], s[26:27], v[2:3] op_sel_hi:[1,0,0]
	v_pk_fma_f32 v[154:155], v[4:5], s[26:27], v[2:3] op_sel_hi:[1,0,0]
	v_exp_f32_e32 v173, v20
	v_exp_f32_e32 v177, v21
	v_exp_f32_e32 v165, v22
	v_exp_f32_e32 v166, v23
	v_exp_f32_e32 v174, v24
	v_exp_f32_e32 v178, v25
	v_exp_f32_e32 v167, v26
	v_exp_f32_e32 v168, v27
	v_exp_f32_e32 v175, v28
	v_exp_f32_e32 v179, v29
	v_exp_f32_e32 v169, v30
	v_exp_f32_e32 v170, v31
	v_exp_f32_e32 v176, v32
	v_exp_f32_e32 v180, v33
	v_exp_f32_e32 v171, v34
	v_exp_f32_e32 v172, v36
	s_or_b32 s4, s4, s8
	v_mov_b32_e32 v16, v3
	v_mov_b32_e32 v17, v3
	v_pk_fma_f32 v[156:157], v[18:19], s[26:27], v[2:3] op_sel_hi:[1,0,0]
	v_pk_fma_f32 v[160:161], v[14:15], s[26:27], v[2:3] op_sel_hi:[1,0,0]
	v_pk_fma_f32 v[124:125], v[12:13], s[26:27], v[2:3] op_sel_hi:[1,0,0]
	v_pk_fma_f32 v[126:127], v[10:11], s[26:27], v[2:3] op_sel_hi:[1,0,0]
	v_pk_fma_f32 v[128:129], v[8:9], s[26:27], v[2:3] op_sel_hi:[1,0,0]
	v_pk_fma_f32 v[130:131], v[6:7], s[26:27], v[2:3] op_sel_hi:[1,0,0]
	s_waitcnt vmcnt(2)
	s_ashr_i32 s5, s4, 31
	v_mov_b32_e32 v2, v3
	v_mov_b32_e32 v6, v3
	v_mov_b32_e32 v7, v3
	v_mov_b32_e32 v8, v3
	v_mov_b32_e32 v9, v3
	v_mov_b32_e32 v10, v3
	v_mov_b32_e32 v11, v3
	v_mov_b32_e32 v12, v3
	v_mov_b32_e32 v13, v3
	v_mov_b32_e32 v14, v3
	v_mov_b32_e32 v15, v3
	s_lshl_b64 s[4:5], s[4:5], 12
	v_lshl_add_u64 v[150:151], v[142:143], 0, s[4:5]
	s_waitcnt vmcnt(3)
	v_mov_b32_e32 v4, v40
	v_mov_b32_e32 v5, v42
	v_mov_b32_e32 v42, v41
	ds_write_b64 v189, v[4:5] offset:16384
	ds_write_b64 v190, v[42:43] offset:16384
	s_waitcnt vmcnt(2)
	ds_write_b128 v191, v[44:47] offset:49152
	v_mov_b32_e32 v4, v3
	v_mov_b32_e32 v5, v3
	v_mov_b64_e32 v[66:67], v[16:17]
	v_mov_b64_e32 v[50:51], v[16:17]
	v_mov_b64_e32 v[34:35], v[16:17]
	v_mov_b64_e32 v[64:65], v[14:15]
	v_mov_b64_e32 v[62:63], v[12:13]
	v_mov_b64_e32 v[60:61], v[10:11]
	v_mov_b64_e32 v[58:59], v[8:9]
	v_mov_b64_e32 v[56:57], v[6:7]
	v_mov_b64_e32 v[54:55], v[4:5]
	v_mov_b64_e32 v[52:53], v[2:3]
	v_mov_b64_e32 v[48:49], v[14:15]
	v_mov_b64_e32 v[46:47], v[12:13]
	v_mov_b64_e32 v[44:45], v[10:11]
	v_mov_b64_e32 v[42:43], v[8:9]
	v_mov_b64_e32 v[40:41], v[6:7]
	v_mov_b64_e32 v[38:39], v[4:5]
	v_mov_b64_e32 v[36:37], v[2:3]
	v_mov_b64_e32 v[32:33], v[14:15]
	v_mov_b64_e32 v[30:31], v[12:13]
	v_mov_b64_e32 v[28:29], v[10:11]
	v_mov_b64_e32 v[26:27], v[8:9]
	v_mov_b64_e32 v[24:25], v[6:7]
	v_mov_b64_e32 v[22:23], v[4:5]
	v_mov_b64_e32 v[20:21], v[2:3]
	v_mov_b64_e32 v[18:19], v[16:17]
	v_mov_b64_e32 v[16:17], v[14:15]
	v_mov_b64_e32 v[14:15], v[12:13]
	v_mov_b64_e32 v[12:13], v[10:11]
	v_mov_b64_e32 v[10:11], v[8:9]
	v_mov_b64_e32 v[8:9], v[6:7]
	v_mov_b64_e32 v[6:7], v[4:5]
	v_mov_b64_e32 v[4:5], v[2:3]
	s_waitcnt lgkmcnt(0)
	s_barrier
	s_waitcnt vmcnt(0)
	ds_read_b128 v[68:71], v192 offset:49152
	ds_read_b128 v[72:75], v193 offset:49152
	v_exp_f32_e32 v154, v154
	v_exp_f32_e32 v155, v155
	v_exp_f32_e32 v130, v130
	v_exp_f32_e32 v131, v131
	v_exp_f32_e32 v128, v128
	v_exp_f32_e32 v129, v129
	v_exp_f32_e32 v126, v126
	v_exp_f32_e32 v127, v127
	v_exp_f32_e32 v124, v124
	v_exp_f32_e32 v125, v125
	v_exp_f32_e32 v160, v160
	v_exp_f32_e32 v161, v161
	v_exp_f32_e32 v158, v158
	v_exp_f32_e32 v159, v159
	v_exp_f32_e32 v156, v156
	v_exp_f32_e32 v157, v157
	v_mul_f32_e32 v216, 0xbe000000, v153
	v_mov_b32_e32 v217, v216
	v_mov_b32_e32 v218, v216
	v_mov_b32_e32 v219, v216
	v_mov_b32_e32 v220, v216
	v_mov_b32_e32 v221, v216
	v_mov_b32_e32 v222, v216
	v_mov_b32_e32 v223, v216
	v_mov_b32_e32 v224, v216
	v_mov_b32_e32 v225, v216
	v_mov_b32_e32 v226, v216
	v_mov_b32_e32 v227, v216
	v_mov_b32_e32 v228, v216
	v_mov_b32_e32 v229, v216
	v_mov_b32_e32 v230, v216
	v_mov_b32_e32 v231, v216
	v_mov_b32_e32 v247, 0x7c7c7c7c
	v_add_f32_e32 v240, v173, v177
	v_add_f32_e32 v240, v165, v240
	v_add_f32_e32 v240, v166, v240
	v_add_f32_e32 v240, v174, v240
	v_add_f32_e32 v240, v178, v240
	v_add_f32_e32 v240, v167, v240
	v_add_f32_e32 v240, v168, v240
	v_add_f32_e32 v240, v175, v240
	v_add_f32_e32 v240, v179, v240
	v_add_f32_e32 v240, v169, v240
	v_add_f32_e32 v240, v170, v240
	v_add_f32_e32 v240, v176, v240
	v_add_f32_e32 v240, v180, v240
	v_add_f32_e32 v240, v171, v240
	v_add_f32_e32 v240, v172, v240
	v_add_f32_e32 v241, v154, v155
	v_add_f32_e32 v241, v130, v241
	v_add_f32_e32 v241, v131, v241
	v_add_f32_e32 v241, v128, v241
	v_add_f32_e32 v241, v129, v241
	v_add_f32_e32 v241, v126, v241
	v_add_f32_e32 v241, v127, v241
	v_add_f32_e32 v241, v124, v241
	v_add_f32_e32 v241, v125, v241
	v_add_f32_e32 v241, v160, v241
	v_add_f32_e32 v241, v161, v241
	v_add_f32_e32 v241, v158, v241
	v_add_f32_e32 v241, v159, v241
	v_add_f32_e32 v241, v156, v241
	v_add_f32_e32 v241, v157, v241
	v_add_f32_e32 v246, v240, v241
	v_mov_b32_e32 v2, v246
	s_nop 0
	s_nop 0
	v_permlane32_swap_b32_e32 v246, v2
	v_add_f32_e32 v246, v246, v2
	v_add_f32_e32 v145, v145, v246
	v_cvt_pk_fp8_f32 v232, v173, v177
	v_cvt_pk_fp8_f32 v233, v174, v178
	v_cvt_pk_fp8_f32 v234, v175, v179
	v_cvt_pk_fp8_f32 v235, v176, v180
	v_cvt_pk_fp8_f32 v232, v165, v166 op_sel:[0,0,1]
	v_cvt_pk_fp8_f32 v233, v167, v168 op_sel:[0,0,1]
	v_cvt_pk_fp8_f32 v234, v169, v170 op_sel:[0,0,1]
	v_cvt_pk_fp8_f32 v235, v171, v172 op_sel:[0,0,1]
	v_cvt_pk_fp8_f32 v236, v154, v155
	v_cvt_pk_fp8_f32 v237, v128, v129
	v_cvt_pk_fp8_f32 v238, v124, v125
	v_cvt_pk_fp8_f32 v239, v158, v159
	v_cvt_pk_fp8_f32 v236, v130, v131 op_sel:[0,0,1]
	v_cvt_pk_fp8_f32 v237, v126, v127 op_sel:[0,0,1]
	v_cvt_pk_fp8_f32 v238, v160, v161 op_sel:[0,0,1]
	v_cvt_pk_fp8_f32 v239, v156, v157 op_sel:[0,0,1]
	v_mov_b32_e32 v156, v116
	v_mov_b32_e32 v157, v117
	v_mov_b32_e32 v158, v118
	v_mov_b32_e32 v159, v119
	v_mov_b32_e32 v160, v120
	v_mov_b32_e32 v161, v121
	v_mov_b32_e32 v162, v122
	v_mov_b32_e32 v163, v123
	v_mov_b32_e32 v254, v156
	v_mov_b32_e32 v255, v158
	ds_write_b64 v189, v[254:255] offset:8192
	v_mov_b32_e32 v244, v157
	v_mov_b32_e32 v245, v159
	ds_write_b64 v190, v[244:245] offset:8192
	ds_write_b128 v191, v[160:163] offset:40960
	global_load_dwordx4 v[180:183], v[150:151], off offset:-64
	v_add_u32_e32 v252, 0xffffe000, v152
	v_mov_b32_e32 v253, v3
	v_lshl_add_u64 v[252:253], v[148:149], 0, v[252:253]
	global_load_dwordx4 v[248:251], v[252:253], off
	ds_read_b128 v[208:211], v194 offset:49152
	ds_read_b128 v[212:215], v195 offset:49152
	ds_read_b128 v[200:203], v192 offset:53248
	ds_read_b128 v[204:207], v193 offset:53248
	s_waitcnt lgkmcnt(4)
	v_mfma_scale_f32_32x32x64_f8f6f4 v[84:99], v[68:75], v[100:107], v[216:231], v188, v247 op_sel_hi:[0,0,0]
	s_waitcnt lgkmcnt(2)
	v_mfma_scale_f32_32x32x64_f8f6f4 v[84:99], v[208:215], v[108:115], v[84:99], v188, v247 op_sel_hi:[0,0,0]
	ds_read_b128 v[208:211], v197 offset:2048
	ds_read_b128 v[212:215], v198 offset:2048
	s_waitcnt lgkmcnt(2)
	v_mfma_scale_f32_32x32x64_f8f6f4 v[68:83], v[200:207], v[100:107], v[216:231], v188, v247 op_sel_hi:[0,0,0]
	ds_read_b128 v[200:203], v194 offset:53248
	ds_read_b128 v[204:207], v195 offset:53248
	s_waitcnt lgkmcnt(0)
	v_mfma_scale_f32_32x32x64_f8f6f4 v[68:83], v[200:207], v[108:115], v[68:83], v188, v247 op_sel_hi:[0,0,0]
	ds_read_b128 v[200:203], v197
	ds_read_b128 v[204:207], v198
	s_waitcnt lgkmcnt(4)
	s_barrier
	s_branch .Lring4_b0
.LBB0_409:
	s_waitcnt vmcnt(0)
	ds_read_b128 v[68:71], v192 offset:49152
	ds_read_b128 v[72:75], v193 offset:49152
	v_mov_b32_e32 v254, v156
	v_mov_b32_e32 v255, v158
	ds_write_b64 v189, v[254:255] offset:8192
	v_mov_b32_e32 v244, v157
	v_mov_b32_e32 v245, v159
	ds_write_b64 v190, v[244:245] offset:8192
	ds_write_b128 v191, v[160:163] offset:40960
	global_load_dwordx4 v[180:183], v[150:151], off offset:-64
	v_add_u32_e32 v252, 0xffffe000, v152
	v_mov_b32_e32 v253, v3
	v_lshl_add_u64 v[252:253], v[148:149], 0, v[252:253]
	global_load_dwordx4 v[248:251], v[252:253], off
	v_exp_f32_e32 v164, v164
	v_exp_f32_e32 v165, v165
	v_exp_f32_e32 v166, v166
	s_waitcnt lgkmcnt(7)
	v_mfma_scale_f32_32x32x64_f8f6f4 v[36:51], v[232:239], v[208:215], v[36:51], v188, v188 op_sel_hi:[0,0,0]
	v_exp_f32_e32 v167, v167
	v_exp_f32_e32 v168, v168
	v_exp_f32_e32 v169, v169
	v_exp_f32_e32 v170, v170
	v_exp_f32_e32 v171, v171
	v_exp_f32_e32 v172, v172
	v_exp_f32_e32 v173, v173
	v_exp_f32_e32 v174, v174
	v_exp_f32_e32 v175, v175
	v_exp_f32_e32 v176, v176
	s_waitcnt lgkmcnt(5)
	v_mfma_scale_f32_32x32x64_f8f6f4 v[52:67], v[232:239], v[200:207], v[52:67], v188, v188 op_sel_hi:[0,0,0]
	ds_read_b128 v[208:211], v197 offset:30720
	ds_read_b128 v[212:215], v198 offset:30720
	ds_read_b128 v[200:203], v197 offset:28672
	ds_read_b128 v[204:207], v198 offset:28672
	v_exp_f32_e32 v177, v177
	v_exp_f32_e32 v178, v178
	v_exp_f32_e32 v179, v179
	v_exp_f32_e32 v116, v116
	v_exp_f32_e32 v117, v117
	v_exp_f32_e32 v118, v118
	v_exp_f32_e32 v119, v119
	v_exp_f32_e32 v120, v120
	v_exp_f32_e32 v121, v121
	v_exp_f32_e32 v122, v122
	s_waitcnt lgkmcnt(2)
	v_mfma_scale_f32_32x32x64_f8f6f4 v[4:19], v[232:239], v[208:215], v[4:19], v188, v188 op_sel_hi:[0,0,0]
	ds_read_b128 v[208:211], v194 offset:49152
	ds_read_b128 v[212:215], v195 offset:49152
	v_exp_f32_e32 v123, v123
	v_exp_f32_e32 v124, v124
	v_exp_f32_e32 v125, v125
	v_exp_f32_e32 v126, v126
	v_exp_f32_e32 v127, v127
	v_exp_f32_e32 v128, v128
	v_exp_f32_e32 v129, v129
	v_exp_f32_e32 v130, v130
	v_exp_f32_e32 v131, v131
	v_add_f32_e32 v240, v164, v165
	s_waitcnt lgkmcnt(2)
	v_mfma_scale_f32_32x32x64_f8f6f4 v[20:35], v[232:239], v[200:207], v[20:35], v188, v188 op_sel_hi:[0,0,0]
	ds_read_b128 v[200:203], v192 offset:53248
	ds_read_b128 v[204:207], v193 offset:53248
	v_add_f32_e32 v241, v116, v117
	v_add_f32_e32 v240, v166, v240
	v_add_f32_e32 v241, v118, v241
	v_add_f32_e32 v240, v167, v240
	v_add_f32_e32 v241, v119, v241
	v_add_f32_e32 v240, v168, v240
	v_add_f32_e32 v241, v120, v241
	v_add_f32_e32 v240, v169, v240
	v_add_f32_e32 v241, v121, v241
	v_add_f32_e32 v240, v170, v240
	v_mfma_scale_f32_32x32x64_f8f6f4 v[84:99], v[68:75], v[100:107], v[216:231], v188, v247 op_sel_hi:[0,0,0]
	v_add_f32_e32 v241, v122, v241
	v_add_f32_e32 v240, v171, v240
	v_add_f32_e32 v241, v123, v241
	v_add_f32_e32 v240, v172, v240
	v_add_f32_e32 v241, v124, v241
	v_add_f32_e32 v240, v173, v240
	v_add_f32_e32 v241, v125, v241
	v_add_f32_e32 v240, v174, v240
	v_add_f32_e32 v241, v126, v241
	v_add_f32_e32 v240, v175, v240
	s_waitcnt lgkmcnt(2)
	v_mfma_scale_f32_32x32x64_f8f6f4 v[84:99], v[208:215], v[108:115], v[84:99], v188, v247 op_sel_hi:[0,0,0]
	ds_read_b128 v[208:211], v197 offset:2048
	ds_read_b128 v[212:215], v198 offset:2048
	v_add_f32_e32 v241, v127, v241
	v_add_f32_e32 v240, v176, v240
	v_add_f32_e32 v241, v128, v241
	v_add_f32_e32 v240, v177, v240
	v_add_f32_e32 v241, v129, v241
	v_add_f32_e32 v240, v178, v240
	v_add_f32_e32 v241, v130, v241
	v_add_f32_e32 v240, v179, v240
	v_add_f32_e32 v241, v131, v241
	v_add_f32_e32 v154, v240, v241
	v_mov_b32_e32 v155, v154
	s_waitcnt lgkmcnt(2)
	v_mfma_scale_f32_32x32x64_f8f6f4 v[68:83], v[200:207], v[100:107], v[216:231], v188, v247 op_sel_hi:[0,0,0]
	ds_read_b128 v[200:203], v194 offset:53248
	ds_read_b128 v[204:207], v195 offset:53248
	v_permlane32_swap_b32_e32 v154, v155
	v_add_f32_e32 v154, v154, v155
	v_add_f32_e32 v145, v145, v154
	v_cvt_pk_fp8_f32 v232, v164, v165
	v_cvt_pk_fp8_f32 v233, v168, v169
	v_cvt_pk_fp8_f32 v234, v172, v173
	v_cvt_pk_fp8_f32 v235, v176, v177
	v_cvt_pk_fp8_f32 v232, v166, v167 op_sel:[0,0,1]
	v_cvt_pk_fp8_f32 v233, v170, v171 op_sel:[0,0,1]
	v_cvt_pk_fp8_f32 v234, v174, v175 op_sel:[0,0,1]
	v_cvt_pk_fp8_f32 v235, v178, v179 op_sel:[0,0,1]
	s_waitcnt lgkmcnt(0)
	v_mfma_scale_f32_32x32x64_f8f6f4 v[68:83], v[200:207], v[108:115], v[68:83], v188, v247 op_sel_hi:[0,0,0]
	ds_read_b128 v[200:203], v197
	ds_read_b128 v[204:207], v198
	v_cvt_pk_fp8_f32 v236, v116, v117
	v_cvt_pk_fp8_f32 v237, v120, v121
	v_cvt_pk_fp8_f32 v238, v124, v125
	v_cvt_pk_fp8_f32 v239, v128, v129
	v_cvt_pk_fp8_f32 v236, v118, v119 op_sel:[0,0,1]
	v_cvt_pk_fp8_f32 v237, v122, v123 op_sel:[0,0,1]
	v_cvt_pk_fp8_f32 v238, v126, v127 op_sel:[0,0,1]
	v_cvt_pk_fp8_f32 v239, v130, v131 op_sel:[0,0,1]
	v_cmp_ge_f32_e32 vcc, 0x43c80000, v154
	s_cmp_eq_u64 vcc, exec
	s_cbranch_scc1 .Lring_norare_a0
	s_nop 15
	s_nop 15
	v_max3_f32 v240, v164, v165, v166
	v_max3_f32 v240, v240, v167, v168
	v_max3_f32 v240, v240, v169, v170
	v_max3_f32 v240, v240, v171, v172
	v_max3_f32 v240, v240, v173, v174
	v_max3_f32 v240, v240, v175, v176
	v_max3_f32 v240, v240, v177, v178
	v_max3_f32 v240, v240, v179, v116
	v_max3_f32 v240, v240, v117, v118
	v_max3_f32 v240, v240, v119, v120
	v_max3_f32 v240, v240, v121, v122
	v_max3_f32 v240, v240, v123, v124
	v_max3_f32 v240, v240, v125, v126
	v_max3_f32 v240, v240, v127, v128
	v_max3_f32 v240, v240, v129, v130
	v_max_f32_e32 v240, v240, v131
	v_mov_b32_e32 v241, v240
	s_nop 1
	v_permlane32_swap_b32_e32 v240, v241
	v_max_f32_e32 v240, v240, v241
	v_log_f32_e32 v2, v240
	s_nop 0
	v_ceil_f32_e32 v2, v2
	v_max_f32_e32 v2, 0, v2
	v_exp_f32_e64 v147, -v2
	s_nop 0
	v_fmamk_f32 v153, v2, 0x41000000, v153
	v_mul_f32_e32 v164, v164, v147
	v_mul_f32_e32 v165, v165, v147
	v_mul_f32_e32 v166, v166, v147
	v_mul_f32_e32 v167, v167, v147
	v_mul_f32_e32 v168, v168, v147
	v_mul_f32_e32 v169, v169, v147
	v_mul_f32_e32 v170, v170, v147
	v_mul_f32_e32 v171, v171, v147
	v_mul_f32_e32 v172, v172, v147
	v_mul_f32_e32 v173, v173, v147
	v_mul_f32_e32 v174, v174, v147
	v_mul_f32_e32 v175, v175, v147
	v_mul_f32_e32 v176, v176, v147
	v_mul_f32_e32 v177, v177, v147
	v_mul_f32_e32 v178, v178, v147
	v_mul_f32_e32 v179, v179, v147
	v_mul_f32_e32 v116, v116, v147
	v_mul_f32_e32 v117, v117, v147
	v_mul_f32_e32 v118, v118, v147
	v_mul_f32_e32 v119, v119, v147
	v_mul_f32_e32 v120, v120, v147
	v_mul_f32_e32 v121, v121, v147
	v_mul_f32_e32 v122, v122, v147
	v_mul_f32_e32 v123, v123, v147
	v_mul_f32_e32 v124, v124, v147
	v_mul_f32_e32 v125, v125, v147
	v_mul_f32_e32 v126, v126, v147
	v_mul_f32_e32 v127, v127, v147
	v_mul_f32_e32 v128, v128, v147
	v_mul_f32_e32 v129, v129, v147
	v_mul_f32_e32 v130, v130, v147
	v_mul_f32_e32 v131, v131, v147
	v_mul_f32_e32 v145, v145, v147
	v_sub_f32_e32 v84, v84, v2
	v_sub_f32_e32 v85, v85, v2
	v_sub_f32_e32 v86, v86, v2
	v_sub_f32_e32 v87, v87, v2
	v_sub_f32_e32 v88, v88, v2
	v_sub_f32_e32 v89, v89, v2
	v_sub_f32_e32 v90, v90, v2
	v_sub_f32_e32 v91, v91, v2
	v_sub_f32_e32 v92, v92, v2
	v_sub_f32_e32 v93, v93, v2
	v_sub_f32_e32 v94, v94, v2
	v_sub_f32_e32 v95, v95, v2
	v_sub_f32_e32 v96, v96, v2
	v_sub_f32_e32 v97, v97, v2
	v_sub_f32_e32 v98, v98, v2
	v_sub_f32_e32 v99, v99, v2
	v_sub_f32_e32 v68, v68, v2
	v_sub_f32_e32 v69, v69, v2
	v_sub_f32_e32 v70, v70, v2
	v_sub_f32_e32 v71, v71, v2
	v_sub_f32_e32 v72, v72, v2
	v_sub_f32_e32 v73, v73, v2
	v_sub_f32_e32 v74, v74, v2
	v_sub_f32_e32 v75, v75, v2
	v_sub_f32_e32 v76, v76, v2
	v_sub_f32_e32 v77, v77, v2
	v_sub_f32_e32 v78, v78, v2
	v_sub_f32_e32 v79, v79, v2
	v_sub_f32_e32 v80, v80, v2
	v_sub_f32_e32 v81, v81, v2
	v_sub_f32_e32 v82, v82, v2
	v_sub_f32_e32 v83, v83, v2
	v_sub_f32_e32 v216, v216, v2
	v_sub_f32_e32 v217, v217, v2
	v_sub_f32_e32 v218, v218, v2
	v_sub_f32_e32 v219, v219, v2
	v_sub_f32_e32 v220, v220, v2
	v_sub_f32_e32 v221, v221, v2
	v_sub_f32_e32 v222, v222, v2
	v_sub_f32_e32 v223, v223, v2
	v_sub_f32_e32 v224, v224, v2
	v_sub_f32_e32 v225, v225, v2
	v_sub_f32_e32 v226, v226, v2
	v_sub_f32_e32 v227, v227, v2
	v_sub_f32_e32 v228, v228, v2
	v_sub_f32_e32 v229, v229, v2
	v_sub_f32_e32 v230, v230, v2
	v_sub_f32_e32 v231, v231, v2
	s_and_saveexec_b64 s[8:9], s[6:7]
	ds_write_b32 v184, v147 offset:128
	s_or_b64 exec, exec, s[8:9]
	s_waitcnt lgkmcnt(0)
	v_add_u32_e32 v253, v135, v185
	ds_read_b128 v[212:215], v253 offset:224
	ds_read_b128 v[208:211], v253 offset:192
	ds_read_b128 v[204:207], v253 offset:160
	ds_read_b128 v[200:203], v253 offset:128
	s_waitcnt lgkmcnt(0)
	v_pk_mul_f32 v[52:53], v[52:53], v[200:201]
	v_pk_mul_f32 v[54:55], v[54:55], v[202:203]
	v_pk_mul_f32 v[56:57], v[56:57], v[204:205]
	v_pk_mul_f32 v[58:59], v[58:59], v[206:207]
	v_pk_mul_f32 v[60:61], v[60:61], v[208:209]
	v_pk_mul_f32 v[62:63], v[62:63], v[210:211]
	v_pk_mul_f32 v[64:65], v[64:65], v[212:213]
	v_pk_mul_f32 v[66:67], v[66:67], v[214:215]
	v_pk_mul_f32 v[36:37], v[36:37], v[200:201]
	v_pk_mul_f32 v[38:39], v[38:39], v[202:203]
	v_pk_mul_f32 v[40:41], v[40:41], v[204:205]
	v_pk_mul_f32 v[42:43], v[42:43], v[206:207]
	v_pk_mul_f32 v[44:45], v[44:45], v[208:209]
	v_pk_mul_f32 v[46:47], v[46:47], v[210:211]
	v_pk_mul_f32 v[48:49], v[48:49], v[212:213]
	v_pk_mul_f32 v[50:51], v[50:51], v[214:215]
	v_pk_mul_f32 v[20:21], v[20:21], v[200:201]
	v_pk_mul_f32 v[22:23], v[22:23], v[202:203]
	v_pk_mul_f32 v[24:25], v[24:25], v[204:205]
	v_pk_mul_f32 v[26:27], v[26:27], v[206:207]
	v_pk_mul_f32 v[28:29], v[28:29], v[208:209]
	v_pk_mul_f32 v[30:31], v[30:31], v[210:211]
	v_pk_mul_f32 v[32:33], v[32:33], v[212:213]
	v_pk_mul_f32 v[34:35], v[34:35], v[214:215]
	v_pk_mul_f32 v[4:5], v[4:5], v[200:201]
	v_pk_mul_f32 v[6:7], v[6:7], v[202:203]
	v_pk_mul_f32 v[8:9], v[8:9], v[204:205]
	v_pk_mul_f32 v[10:11], v[10:11], v[206:207]
	v_pk_mul_f32 v[12:13], v[12:13], v[208:209]
	v_pk_mul_f32 v[14:15], v[14:15], v[210:211]
	v_pk_mul_f32 v[16:17], v[16:17], v[212:213]
	v_pk_mul_f32 v[18:19], v[18:19], v[214:215]
	v_cvt_pk_fp8_f32 v232, v164, v165
	v_cvt_pk_fp8_f32 v233, v168, v169
	v_cvt_pk_fp8_f32 v234, v172, v173
	v_cvt_pk_fp8_f32 v235, v176, v177
	v_cvt_pk_fp8_f32 v232, v166, v167 op_sel:[0,0,1]
	v_cvt_pk_fp8_f32 v233, v170, v171 op_sel:[0,0,1]
	v_cvt_pk_fp8_f32 v234, v174, v175 op_sel:[0,0,1]
	v_cvt_pk_fp8_f32 v235, v178, v179 op_sel:[0,0,1]
	v_cvt_pk_fp8_f32 v236, v116, v117
	v_cvt_pk_fp8_f32 v237, v120, v121
	v_cvt_pk_fp8_f32 v238, v124, v125
	v_cvt_pk_fp8_f32 v239, v128, v129
	v_cvt_pk_fp8_f32 v236, v118, v119 op_sel:[0,0,1]
	v_cvt_pk_fp8_f32 v237, v122, v123 op_sel:[0,0,1]
	v_cvt_pk_fp8_f32 v238, v126, v127 op_sel:[0,0,1]
	v_cvt_pk_fp8_f32 v239, v130, v131 op_sel:[0,0,1]
	ds_read_b128 v[208:211], v197 offset:2048
	ds_read_b128 v[212:215], v198 offset:2048
	ds_read_b128 v[200:203], v197
	ds_read_b128 v[204:207], v198
.Lring_norare_a0:
	s_waitcnt lgkmcnt(4)
	s_barrier
.Lring4_b0:
	s_waitcnt vmcnt(0)
	s_cmp_gt_u32 s15, 60
	s_cselect_b64 s[8:9], -1, 0
	s_and_b64 vcc, exec, s[8:9]
	s_cbranch_vccnz .Lring_noload_b0
	v_mov_b32_e32 v252, v152
	v_mov_b32_e32 v253, v3
	v_lshl_add_u64 v[252:253], v[148:149], 0, v[252:253]
	global_load_dwordx4 v[156:159], v[150:151], off
	s_nop 0
	global_load_dwordx4 v[160:163], v[252:253], off
.Lring_noload_b0:
	ds_read_b128 v[116:119], v192 offset:40960
	ds_read_b128 v[120:123], v193 offset:40960
	v_mov_b32_e32 v254, v180
	v_mov_b32_e32 v255, v182
	ds_write_b64 v189, v[254:255] offset:24576
	v_mov_b32_e32 v244, v181
	v_mov_b32_e32 v245, v183
	ds_write_b64 v190, v[244:245] offset:24576
	ds_write_b128 v191, v[248:251] offset:57344
	v_exp_f32_e32 v84, v84
	v_exp_f32_e32 v85, v85
	v_exp_f32_e32 v86, v86
	v_exp_f32_e32 v87, v87
	v_exp_f32_e32 v88, v88
	v_exp_f32_e32 v89, v89
	s_waitcnt lgkmcnt(7)
	v_mfma_scale_f32_32x32x64_f8f6f4 v[36:51], v[232:239], v[208:215], v[36:51], v188, v188 op_sel_hi:[0,0,0]
	v_exp_f32_e32 v90, v90
	v_exp_f32_e32 v91, v91
	v_exp_f32_e32 v92, v92
	v_exp_f32_e32 v93, v93
	v_exp_f32_e32 v94, v94
	v_exp_f32_e32 v95, v95
	v_exp_f32_e32 v96, v96
	v_exp_f32_e32 v97, v97
	v_exp_f32_e32 v98, v98
	v_exp_f32_e32 v99, v99
	s_waitcnt lgkmcnt(5)
	v_mfma_scale_f32_32x32x64_f8f6f4 v[52:67], v[232:239], v[200:207], v[52:67], v188, v188 op_sel_hi:[0,0,0]
	ds_read_b128 v[208:211], v197 offset:6144
	ds_read_b128 v[212:215], v198 offset:6144
	ds_read_b128 v[200:203], v197 offset:4096
	ds_read_b128 v[204:207], v198 offset:4096
	v_exp_f32_e32 v68, v68
	v_exp_f32_e32 v69, v69
	v_exp_f32_e32 v70, v70
	v_exp_f32_e32 v71, v71
	v_exp_f32_e32 v72, v72
	v_exp_f32_e32 v73, v73
	v_exp_f32_e32 v74, v74
	v_exp_f32_e32 v75, v75
	v_exp_f32_e32 v76, v76
	v_exp_f32_e32 v77, v77
	s_waitcnt lgkmcnt(2)
	v_mfma_scale_f32_32x32x64_f8f6f4 v[4:19], v[232:239], v[208:215], v[4:19], v188, v188 op_sel_hi:[0,0,0]
	ds_read_b128 v[208:211], v194 offset:40960
	ds_read_b128 v[212:215], v195 offset:40960
	v_exp_f32_e32 v78, v78
	v_exp_f32_e32 v79, v79
	v_exp_f32_e32 v80, v80
	v_exp_f32_e32 v81, v81
	v_exp_f32_e32 v82, v82
	v_exp_f32_e32 v83, v83
	v_add_f32_e32 v240, v84, v85
	v_add_f32_e32 v241, v68, v69
	v_add_f32_e32 v240, v86, v240
	v_add_f32_e32 v241, v70, v241
	s_waitcnt lgkmcnt(2)
	v_mfma_scale_f32_32x32x64_f8f6f4 v[20:35], v[232:239], v[200:207], v[20:35], v188, v188 op_sel_hi:[0,0,0]
	ds_read_b128 v[200:203], v192 offset:45056
	ds_read_b128 v[204:207], v193 offset:45056
	v_add_f32_e32 v240, v87, v240
	v_add_f32_e32 v241, v71, v241
	v_add_f32_e32 v240, v88, v240
	v_add_f32_e32 v241, v72, v241
	v_add_f32_e32 v240, v89, v240
	v_add_f32_e32 v241, v73, v241
	v_add_f32_e32 v240, v90, v240
	v_add_f32_e32 v241, v74, v241
	v_add_f32_e32 v240, v91, v240
	v_add_f32_e32 v241, v75, v241
	v_mfma_scale_f32_32x32x64_f8f6f4 v[164:179], v[116:123], v[100:107], v[216:231], v188, v247 op_sel_hi:[0,0,0]
	v_add_f32_e32 v240, v92, v240
	v_add_f32_e32 v241, v76, v241
	v_add_f32_e32 v240, v93, v240
	v_add_f32_e32 v241, v77, v241
	v_add_f32_e32 v240, v94, v240
	v_add_f32_e32 v241, v78, v241
	v_add_f32_e32 v240, v95, v240
	v_add_f32_e32 v241, v79, v241
	v_add_f32_e32 v240, v96, v240
	v_add_f32_e32 v241, v80, v241
	s_waitcnt lgkmcnt(2)
	v_mfma_scale_f32_32x32x64_f8f6f4 v[164:179], v[208:215], v[108:115], v[164:179], v188, v247 op_sel_hi:[0,0,0]
	ds_read_b128 v[208:211], v197 offset:18432
	ds_read_b128 v[212:215], v198 offset:18432
	v_add_f32_e32 v240, v97, v240
	v_add_f32_e32 v241, v81, v241
	v_add_f32_e32 v240, v98, v240
	v_add_f32_e32 v241, v82, v241
	v_add_f32_e32 v240, v99, v240
	v_add_f32_e32 v241, v83, v241
	v_add_f32_e32 v154, v240, v241
	v_mov_b32_e32 v155, v154
	s_nop 0
	s_nop 0
	v_permlane32_swap_b32_e32 v154, v155
	v_add_f32_e32 v154, v154, v155
	s_waitcnt lgkmcnt(2)
	v_mfma_scale_f32_32x32x64_f8f6f4 v[116:131], v[200:207], v[100:107], v[216:231], v188, v247 op_sel_hi:[0,0,0]
	ds_read_b128 v[200:203], v194 offset:45056
	ds_read_b128 v[204:207], v195 offset:45056
	v_add_f32_e32 v145, v145, v154
	v_cvt_pk_fp8_f32 v232, v84, v85
	v_cvt_pk_fp8_f32 v233, v88, v89
	v_cvt_pk_fp8_f32 v234, v92, v93
	v_cvt_pk_fp8_f32 v235, v96, v97
	v_cvt_pk_fp8_f32 v232, v86, v87 op_sel:[0,0,1]
	v_cvt_pk_fp8_f32 v233, v90, v91 op_sel:[0,0,1]
	v_cvt_pk_fp8_f32 v234, v94, v95 op_sel:[0,0,1]
	v_cvt_pk_fp8_f32 v235, v98, v99 op_sel:[0,0,1]
	v_cvt_pk_fp8_f32 v236, v68, v69
	s_waitcnt lgkmcnt(0)
	v_mfma_scale_f32_32x32x64_f8f6f4 v[116:131], v[200:207], v[108:115], v[116:131], v188, v247 op_sel_hi:[0,0,0]
	ds_read_b128 v[200:203], v197 offset:16384
	ds_read_b128 v[204:207], v198 offset:16384
	v_cvt_pk_fp8_f32 v237, v72, v73
	v_cvt_pk_fp8_f32 v238, v76, v77
	v_cvt_pk_fp8_f32 v239, v80, v81
	v_cvt_pk_fp8_f32 v236, v70, v71 op_sel:[0,0,1]
	v_cvt_pk_fp8_f32 v237, v74, v75 op_sel:[0,0,1]
	v_cvt_pk_fp8_f32 v238, v78, v79 op_sel:[0,0,1]
	v_cvt_pk_fp8_f32 v239, v82, v83 op_sel:[0,0,1]
	v_cmp_ge_f32_e32 vcc, 0x43c80000, v154
	s_cmp_eq_u64 vcc, exec
	s_cbranch_scc1 .Lring_norare_b0
	s_nop 15
	s_nop 15
	v_max3_f32 v240, v84, v85, v86
	v_max3_f32 v240, v240, v87, v88
	v_max3_f32 v240, v240, v89, v90
	v_max3_f32 v240, v240, v91, v92
	v_max3_f32 v240, v240, v93, v94
	v_max3_f32 v240, v240, v95, v96
	v_max3_f32 v240, v240, v97, v98
	v_max3_f32 v240, v240, v99, v68
	v_max3_f32 v240, v240, v69, v70
	v_max3_f32 v240, v240, v71, v72
	v_max3_f32 v240, v240, v73, v74
	v_max3_f32 v240, v240, v75, v76
	v_max3_f32 v240, v240, v77, v78
	v_max3_f32 v240, v240, v79, v80
	v_max3_f32 v240, v240, v81, v82
	v_max_f32_e32 v240, v240, v83
	v_mov_b32_e32 v241, v240
	s_nop 1
	v_permlane32_swap_b32_e32 v240, v241
	v_max_f32_e32 v240, v240, v241
	v_log_f32_e32 v2, v240
	s_nop 0
	v_ceil_f32_e32 v2, v2
	v_max_f32_e32 v2, 0, v2
	v_exp_f32_e64 v147, -v2
	s_nop 0
	v_fmamk_f32 v153, v2, 0x41000000, v153
	v_mul_f32_e32 v84, v84, v147
	v_mul_f32_e32 v85, v85, v147
	v_mul_f32_e32 v86, v86, v147
	v_mul_f32_e32 v87, v87, v147
	v_mul_f32_e32 v88, v88, v147
	v_mul_f32_e32 v89, v89, v147
	v_mul_f32_e32 v90, v90, v147
	v_mul_f32_e32 v91, v91, v147
	v_mul_f32_e32 v92, v92, v147
	v_mul_f32_e32 v93, v93, v147
	v_mul_f32_e32 v94, v94, v147
	v_mul_f32_e32 v95, v95, v147
	v_mul_f32_e32 v96, v96, v147
	v_mul_f32_e32 v97, v97, v147
	v_mul_f32_e32 v98, v98, v147
	v_mul_f32_e32 v99, v99, v147
	v_mul_f32_e32 v68, v68, v147
	v_mul_f32_e32 v69, v69, v147
	v_mul_f32_e32 v70, v70, v147
	v_mul_f32_e32 v71, v71, v147
	v_mul_f32_e32 v72, v72, v147
	v_mul_f32_e32 v73, v73, v147
	v_mul_f32_e32 v74, v74, v147
	v_mul_f32_e32 v75, v75, v147
	v_mul_f32_e32 v76, v76, v147
	v_mul_f32_e32 v77, v77, v147
	v_mul_f32_e32 v78, v78, v147
	v_mul_f32_e32 v79, v79, v147
	v_mul_f32_e32 v80, v80, v147
	v_mul_f32_e32 v81, v81, v147
	v_mul_f32_e32 v82, v82, v147
	v_mul_f32_e32 v83, v83, v147
	v_mul_f32_e32 v145, v145, v147
	v_sub_f32_e32 v164, v164, v2
	v_sub_f32_e32 v165, v165, v2
	v_sub_f32_e32 v166, v166, v2
	v_sub_f32_e32 v167, v167, v2
	v_sub_f32_e32 v168, v168, v2
	v_sub_f32_e32 v169, v169, v2
	v_sub_f32_e32 v170, v170, v2
	v_sub_f32_e32 v171, v171, v2
	v_sub_f32_e32 v172, v172, v2
	v_sub_f32_e32 v173, v173, v2
	v_sub_f32_e32 v174, v174, v2
	v_sub_f32_e32 v175, v175, v2
	v_sub_f32_e32 v176, v176, v2
	v_sub_f32_e32 v177, v177, v2
	v_sub_f32_e32 v178, v178, v2
	v_sub_f32_e32 v179, v179, v2
	v_sub_f32_e32 v116, v116, v2
	v_sub_f32_e32 v117, v117, v2
	v_sub_f32_e32 v118, v118, v2
	v_sub_f32_e32 v119, v119, v2
	v_sub_f32_e32 v120, v120, v2
	v_sub_f32_e32 v121, v121, v2
	v_sub_f32_e32 v122, v122, v2
	v_sub_f32_e32 v123, v123, v2
	v_sub_f32_e32 v124, v124, v2
	v_sub_f32_e32 v125, v125, v2
	v_sub_f32_e32 v126, v126, v2
	v_sub_f32_e32 v127, v127, v2
	v_sub_f32_e32 v128, v128, v2
	v_sub_f32_e32 v129, v129, v2
	v_sub_f32_e32 v130, v130, v2
	v_sub_f32_e32 v131, v131, v2
	v_sub_f32_e32 v216, v216, v2
	v_sub_f32_e32 v217, v217, v2
	v_sub_f32_e32 v218, v218, v2
	v_sub_f32_e32 v219, v219, v2
	v_sub_f32_e32 v220, v220, v2
	v_sub_f32_e32 v221, v221, v2
	v_sub_f32_e32 v222, v222, v2
	v_sub_f32_e32 v223, v223, v2
	v_sub_f32_e32 v224, v224, v2
	v_sub_f32_e32 v225, v225, v2
	v_sub_f32_e32 v226, v226, v2
	v_sub_f32_e32 v227, v227, v2
	v_sub_f32_e32 v228, v228, v2
	v_sub_f32_e32 v229, v229, v2
	v_sub_f32_e32 v230, v230, v2
	v_sub_f32_e32 v231, v231, v2
	s_and_saveexec_b64 s[10:11], s[6:7]
	ds_write_b32 v184, v147 offset:128
	s_or_b64 exec, exec, s[10:11]
	s_waitcnt lgkmcnt(0)
	v_add_u32_e32 v253, v135, v185
	ds_read_b128 v[212:215], v253 offset:224
	ds_read_b128 v[208:211], v253 offset:192
	ds_read_b128 v[204:207], v253 offset:160
	ds_read_b128 v[200:203], v253 offset:128
	s_waitcnt lgkmcnt(0)
	v_pk_mul_f32 v[52:53], v[52:53], v[200:201]
	v_pk_mul_f32 v[54:55], v[54:55], v[202:203]
	v_pk_mul_f32 v[56:57], v[56:57], v[204:205]
	v_pk_mul_f32 v[58:59], v[58:59], v[206:207]
	v_pk_mul_f32 v[60:61], v[60:61], v[208:209]
	v_pk_mul_f32 v[62:63], v[62:63], v[210:211]
	v_pk_mul_f32 v[64:65], v[64:65], v[212:213]
	v_pk_mul_f32 v[66:67], v[66:67], v[214:215]
	v_pk_mul_f32 v[36:37], v[36:37], v[200:201]
	v_pk_mul_f32 v[38:39], v[38:39], v[202:203]
	v_pk_mul_f32 v[40:41], v[40:41], v[204:205]
	v_pk_mul_f32 v[42:43], v[42:43], v[206:207]
	v_pk_mul_f32 v[44:45], v[44:45], v[208:209]
	v_pk_mul_f32 v[46:47], v[46:47], v[210:211]
	v_pk_mul_f32 v[48:49], v[48:49], v[212:213]
	v_pk_mul_f32 v[50:51], v[50:51], v[214:215]
	v_pk_mul_f32 v[20:21], v[20:21], v[200:201]
	v_pk_mul_f32 v[22:23], v[22:23], v[202:203]
	v_pk_mul_f32 v[24:25], v[24:25], v[204:205]
	v_pk_mul_f32 v[26:27], v[26:27], v[206:207]
	v_pk_mul_f32 v[28:29], v[28:29], v[208:209]
	v_pk_mul_f32 v[30:31], v[30:31], v[210:211]
	v_pk_mul_f32 v[32:33], v[32:33], v[212:213]
	v_pk_mul_f32 v[34:35], v[34:35], v[214:215]
	v_pk_mul_f32 v[4:5], v[4:5], v[200:201]
	v_pk_mul_f32 v[6:7], v[6:7], v[202:203]
	v_pk_mul_f32 v[8:9], v[8:9], v[204:205]
	v_pk_mul_f32 v[10:11], v[10:11], v[206:207]
	v_pk_mul_f32 v[12:13], v[12:13], v[208:209]
	v_pk_mul_f32 v[14:15], v[14:15], v[210:211]
	v_pk_mul_f32 v[16:17], v[16:17], v[212:213]
	v_pk_mul_f32 v[18:19], v[18:19], v[214:215]
	v_cvt_pk_fp8_f32 v232, v84, v85
	v_cvt_pk_fp8_f32 v233, v88, v89
	v_cvt_pk_fp8_f32 v234, v92, v93
	v_cvt_pk_fp8_f32 v235, v96, v97
	v_cvt_pk_fp8_f32 v232, v86, v87 op_sel:[0,0,1]
	v_cvt_pk_fp8_f32 v233, v90, v91 op_sel:[0,0,1]
	v_cvt_pk_fp8_f32 v234, v94, v95 op_sel:[0,0,1]
	v_cvt_pk_fp8_f32 v235, v98, v99 op_sel:[0,0,1]
	v_cvt_pk_fp8_f32 v236, v68, v69
	v_cvt_pk_fp8_f32 v237, v72, v73
	v_cvt_pk_fp8_f32 v238, v76, v77
	v_cvt_pk_fp8_f32 v239, v80, v81
	v_cvt_pk_fp8_f32 v236, v70, v71 op_sel:[0,0,1]
	v_cvt_pk_fp8_f32 v237, v74, v75 op_sel:[0,0,1]
	v_cvt_pk_fp8_f32 v238, v78, v79 op_sel:[0,0,1]
	v_cvt_pk_fp8_f32 v239, v82, v83 op_sel:[0,0,1]
	ds_read_b128 v[208:211], v197 offset:18432
	ds_read_b128 v[212:215], v198 offset:18432
	ds_read_b128 v[200:203], v197 offset:16384
	ds_read_b128 v[204:207], v198 offset:16384
.Lring_norare_b0:
	s_add_i32 s15, s15, 2
	v_lshl_add_u64 v[150:151], v[150:151], 0, s[28:29]
	v_add_u32_e32 v152, 0x4000, v152
	s_and_b64 vcc, exec, s[8:9]
	s_waitcnt lgkmcnt(4)
	s_barrier
	s_cbranch_vccnz .Lring_drain_b0
	s_waitcnt vmcnt(0)
	ds_read_b128 v[68:71], v192 offset:57344
	ds_read_b128 v[72:75], v193 offset:57344
	v_mov_b32_e32 v254, v156
	v_mov_b32_e32 v255, v158
	ds_write_b64 v189, v[254:255]
	v_mov_b32_e32 v244, v157
	v_mov_b32_e32 v245, v159
	ds_write_b64 v190, v[244:245]
	ds_write_b128 v191, v[160:163] offset:32768
	global_load_dwordx4 v[180:183], v[150:151], off offset:-64
	v_add_u32_e32 v252, 0xffffe000, v152
	v_mov_b32_e32 v253, v3
	v_lshl_add_u64 v[252:253], v[148:149], 0, v[252:253]
	global_load_dwordx4 v[248:251], v[252:253], off
	v_exp_f32_e32 v164, v164
	v_exp_f32_e32 v165, v165
	v_exp_f32_e32 v166, v166
	s_waitcnt lgkmcnt(7)
	v_mfma_scale_f32_32x32x64_f8f6f4 v[36:51], v[232:239], v[208:215], v[36:51], v188, v188 op_sel_hi:[0,0,0]
	v_exp_f32_e32 v167, v167
	v_exp_f32_e32 v168, v168
	v_exp_f32_e32 v169, v169
	v_exp_f32_e32 v170, v170
	v_exp_f32_e32 v171, v171
	v_exp_f32_e32 v172, v172
	v_exp_f32_e32 v173, v173
	v_exp_f32_e32 v174, v174
	v_exp_f32_e32 v175, v175
	v_exp_f32_e32 v176, v176
	s_waitcnt lgkmcnt(5)
	v_mfma_scale_f32_32x32x64_f8f6f4 v[52:67], v[232:239], v[200:207], v[52:67], v188, v188 op_sel_hi:[0,0,0]
	ds_read_b128 v[208:211], v197 offset:22528
	ds_read_b128 v[212:215], v198 offset:22528
	ds_read_b128 v[200:203], v197 offset:20480
	ds_read_b128 v[204:207], v198 offset:20480
	v_exp_f32_e32 v177, v177
	v_exp_f32_e32 v178, v178
	v_exp_f32_e32 v179, v179
	v_exp_f32_e32 v116, v116
	v_exp_f32_e32 v117, v117
	v_exp_f32_e32 v118, v118
	v_exp_f32_e32 v119, v119
	v_exp_f32_e32 v120, v120
	v_exp_f32_e32 v121, v121
	v_exp_f32_e32 v122, v122
	s_waitcnt lgkmcnt(2)
	v_mfma_scale_f32_32x32x64_f8f6f4 v[4:19], v[232:239], v[208:215], v[4:19], v188, v188 op_sel_hi:[0,0,0]
	ds_read_b128 v[208:211], v194 offset:57344
	ds_read_b128 v[212:215], v195 offset:57344
	v_exp_f32_e32 v123, v123
	v_exp_f32_e32 v124, v124
	v_exp_f32_e32 v125, v125
	v_exp_f32_e32 v126, v126
	v_exp_f32_e32 v127, v127
	v_exp_f32_e32 v128, v128
	v_exp_f32_e32 v129, v129
	v_exp_f32_e32 v130, v130
	v_exp_f32_e32 v131, v131
	v_add_f32_e32 v240, v164, v165
	s_waitcnt lgkmcnt(2)
	v_mfma_scale_f32_32x32x64_f8f6f4 v[20:35], v[232:239], v[200:207], v[20:35], v188, v188 op_sel_hi:[0,0,0]
	ds_read_b128 v[200:203], v192 offset:61440
	ds_read_b128 v[204:207], v193 offset:61440
	v_add_f32_e32 v241, v116, v117
	v_add_f32_e32 v240, v166, v240
	v_add_f32_e32 v241, v118, v241
	v_add_f32_e32 v240, v167, v240
	v_add_f32_e32 v241, v119, v241
	v_add_f32_e32 v240, v168, v240
	v_add_f32_e32 v241, v120, v241
	v_add_f32_e32 v240, v169, v240
	v_add_f32_e32 v241, v121, v241
	v_add_f32_e32 v240, v170, v240
	v_mfma_scale_f32_32x32x64_f8f6f4 v[84:99], v[68:75], v[100:107], v[216:231], v188, v247 op_sel_hi:[0,0,0]
	v_add_f32_e32 v241, v122, v241
	v_add_f32_e32 v240, v171, v240
	v_add_f32_e32 v241, v123, v241
	v_add_f32_e32 v240, v172, v240
	v_add_f32_e32 v241, v124, v241
	v_add_f32_e32 v240, v173, v240
	v_add_f32_e32 v241, v125, v241
	v_add_f32_e32 v240, v174, v240
	v_add_f32_e32 v241, v126, v241
	v_add_f32_e32 v240, v175, v240
	s_waitcnt lgkmcnt(2)
	v_mfma_scale_f32_32x32x64_f8f6f4 v[84:99], v[208:215], v[108:115], v[84:99], v188, v247 op_sel_hi:[0,0,0]
	ds_read_b128 v[208:211], v197 offset:10240
	ds_read_b128 v[212:215], v198 offset:10240
	v_add_f32_e32 v241, v127, v241
	v_add_f32_e32 v240, v176, v240
	v_add_f32_e32 v241, v128, v241
	v_add_f32_e32 v240, v177, v240
	v_add_f32_e32 v241, v129, v241
	v_add_f32_e32 v240, v178, v240
	v_add_f32_e32 v241, v130, v241
	v_add_f32_e32 v240, v179, v240
	v_add_f32_e32 v241, v131, v241
	v_add_f32_e32 v154, v240, v241
	v_mov_b32_e32 v155, v154
	s_waitcnt lgkmcnt(2)
	v_mfma_scale_f32_32x32x64_f8f6f4 v[68:83], v[200:207], v[100:107], v[216:231], v188, v247 op_sel_hi:[0,0,0]
	ds_read_b128 v[200:203], v194 offset:61440
	ds_read_b128 v[204:207], v195 offset:61440
	v_permlane32_swap_b32_e32 v154, v155
	v_add_f32_e32 v154, v154, v155
	v_add_f32_e32 v145, v145, v154
	v_cvt_pk_fp8_f32 v232, v164, v165
	v_cvt_pk_fp8_f32 v233, v168, v169
	v_cvt_pk_fp8_f32 v234, v172, v173
	v_cvt_pk_fp8_f32 v235, v176, v177
	v_cvt_pk_fp8_f32 v232, v166, v167 op_sel:[0,0,1]
	v_cvt_pk_fp8_f32 v233, v170, v171 op_sel:[0,0,1]
	v_cvt_pk_fp8_f32 v234, v174, v175 op_sel:[0,0,1]
	v_cvt_pk_fp8_f32 v235, v178, v179 op_sel:[0,0,1]
	s_waitcnt lgkmcnt(0)
	v_mfma_scale_f32_32x32x64_f8f6f4 v[68:83], v[200:207], v[108:115], v[68:83], v188, v247 op_sel_hi:[0,0,0]
	ds_read_b128 v[200:203], v197 offset:8192
	ds_read_b128 v[204:207], v198 offset:8192
	v_cvt_pk_fp8_f32 v236, v116, v117
	v_cvt_pk_fp8_f32 v237, v120, v121
	v_cvt_pk_fp8_f32 v238, v124, v125
	v_cvt_pk_fp8_f32 v239, v128, v129
	v_cvt_pk_fp8_f32 v236, v118, v119 op_sel:[0,0,1]
	v_cvt_pk_fp8_f32 v237, v122, v123 op_sel:[0,0,1]
	v_cvt_pk_fp8_f32 v238, v126, v127 op_sel:[0,0,1]
	v_cvt_pk_fp8_f32 v239, v130, v131 op_sel:[0,0,1]
	v_cmp_ge_f32_e32 vcc, 0x43c80000, v154
	s_cmp_eq_u64 vcc, exec
	s_cbranch_scc1 .Lring_norare_a1
	s_nop 15
	s_nop 15
	v_max3_f32 v240, v164, v165, v166
	v_max3_f32 v240, v240, v167, v168
	v_max3_f32 v240, v240, v169, v170
	v_max3_f32 v240, v240, v171, v172
	v_max3_f32 v240, v240, v173, v174
	v_max3_f32 v240, v240, v175, v176
	v_max3_f32 v240, v240, v177, v178
	v_max3_f32 v240, v240, v179, v116
	v_max3_f32 v240, v240, v117, v118
	v_max3_f32 v240, v240, v119, v120
	v_max3_f32 v240, v240, v121, v122
	v_max3_f32 v240, v240, v123, v124
	v_max3_f32 v240, v240, v125, v126
	v_max3_f32 v240, v240, v127, v128
	v_max3_f32 v240, v240, v129, v130
	v_max_f32_e32 v240, v240, v131
	v_mov_b32_e32 v241, v240
	s_nop 1
	v_permlane32_swap_b32_e32 v240, v241
	v_max_f32_e32 v240, v240, v241
	v_log_f32_e32 v2, v240
	s_nop 0
	v_ceil_f32_e32 v2, v2
	v_max_f32_e32 v2, 0, v2
	v_exp_f32_e64 v147, -v2
	s_nop 0
	v_fmamk_f32 v153, v2, 0x41000000, v153
	v_mul_f32_e32 v164, v164, v147
	v_mul_f32_e32 v165, v165, v147
	v_mul_f32_e32 v166, v166, v147
	v_mul_f32_e32 v167, v167, v147
	v_mul_f32_e32 v168, v168, v147
	v_mul_f32_e32 v169, v169, v147
	v_mul_f32_e32 v170, v170, v147
	v_mul_f32_e32 v171, v171, v147
	v_mul_f32_e32 v172, v172, v147
	v_mul_f32_e32 v173, v173, v147
	v_mul_f32_e32 v174, v174, v147
	v_mul_f32_e32 v175, v175, v147
	v_mul_f32_e32 v176, v176, v147
	v_mul_f32_e32 v177, v177, v147
	v_mul_f32_e32 v178, v178, v147
	v_mul_f32_e32 v179, v179, v147
	v_mul_f32_e32 v116, v116, v147
	v_mul_f32_e32 v117, v117, v147
	v_mul_f32_e32 v118, v118, v147
	v_mul_f32_e32 v119, v119, v147
	v_mul_f32_e32 v120, v120, v147
	v_mul_f32_e32 v121, v121, v147
	v_mul_f32_e32 v122, v122, v147
	v_mul_f32_e32 v123, v123, v147
	v_mul_f32_e32 v124, v124, v147
	v_mul_f32_e32 v125, v125, v147
	v_mul_f32_e32 v126, v126, v147
	v_mul_f32_e32 v127, v127, v147
	v_mul_f32_e32 v128, v128, v147
	v_mul_f32_e32 v129, v129, v147
	v_mul_f32_e32 v130, v130, v147
	v_mul_f32_e32 v131, v131, v147
	v_mul_f32_e32 v145, v145, v147
	v_sub_f32_e32 v84, v84, v2
	v_sub_f32_e32 v85, v85, v2
	v_sub_f32_e32 v86, v86, v2
	v_sub_f32_e32 v87, v87, v2
	v_sub_f32_e32 v88, v88, v2
	v_sub_f32_e32 v89, v89, v2
	v_sub_f32_e32 v90, v90, v2
	v_sub_f32_e32 v91, v91, v2
	v_sub_f32_e32 v92, v92, v2
	v_sub_f32_e32 v93, v93, v2
	v_sub_f32_e32 v94, v94, v2
	v_sub_f32_e32 v95, v95, v2
	v_sub_f32_e32 v96, v96, v2
	v_sub_f32_e32 v97, v97, v2
	v_sub_f32_e32 v98, v98, v2
	v_sub_f32_e32 v99, v99, v2
	v_sub_f32_e32 v68, v68, v2
	v_sub_f32_e32 v69, v69, v2
	v_sub_f32_e32 v70, v70, v2
	v_sub_f32_e32 v71, v71, v2
	v_sub_f32_e32 v72, v72, v2
	v_sub_f32_e32 v73, v73, v2
	v_sub_f32_e32 v74, v74, v2
	v_sub_f32_e32 v75, v75, v2
	v_sub_f32_e32 v76, v76, v2
	v_sub_f32_e32 v77, v77, v2
	v_sub_f32_e32 v78, v78, v2
	v_sub_f32_e32 v79, v79, v2
	v_sub_f32_e32 v80, v80, v2
	v_sub_f32_e32 v81, v81, v2
	v_sub_f32_e32 v82, v82, v2
	v_sub_f32_e32 v83, v83, v2
	v_sub_f32_e32 v216, v216, v2
	v_sub_f32_e32 v217, v217, v2
	v_sub_f32_e32 v218, v218, v2
	v_sub_f32_e32 v219, v219, v2
	v_sub_f32_e32 v220, v220, v2
	v_sub_f32_e32 v221, v221, v2
	v_sub_f32_e32 v222, v222, v2
	v_sub_f32_e32 v223, v223, v2
	v_sub_f32_e32 v224, v224, v2
	v_sub_f32_e32 v225, v225, v2
	v_sub_f32_e32 v226, v226, v2
	v_sub_f32_e32 v227, v227, v2
	v_sub_f32_e32 v228, v228, v2
	v_sub_f32_e32 v229, v229, v2
	v_sub_f32_e32 v230, v230, v2
	v_sub_f32_e32 v231, v231, v2
	s_and_saveexec_b64 s[8:9], s[6:7]
	ds_write_b32 v184, v147 offset:128
	s_or_b64 exec, exec, s[8:9]
	s_waitcnt lgkmcnt(0)
	v_add_u32_e32 v253, v135, v185
	ds_read_b128 v[212:215], v253 offset:224
	ds_read_b128 v[208:211], v253 offset:192
	ds_read_b128 v[204:207], v253 offset:160
	ds_read_b128 v[200:203], v253 offset:128
	s_waitcnt lgkmcnt(0)
	v_pk_mul_f32 v[52:53], v[52:53], v[200:201]
	v_pk_mul_f32 v[54:55], v[54:55], v[202:203]
	v_pk_mul_f32 v[56:57], v[56:57], v[204:205]
	v_pk_mul_f32 v[58:59], v[58:59], v[206:207]
	v_pk_mul_f32 v[60:61], v[60:61], v[208:209]
	v_pk_mul_f32 v[62:63], v[62:63], v[210:211]
	v_pk_mul_f32 v[64:65], v[64:65], v[212:213]
	v_pk_mul_f32 v[66:67], v[66:67], v[214:215]
	v_pk_mul_f32 v[36:37], v[36:37], v[200:201]
	v_pk_mul_f32 v[38:39], v[38:39], v[202:203]
	v_pk_mul_f32 v[40:41], v[40:41], v[204:205]
	v_pk_mul_f32 v[42:43], v[42:43], v[206:207]
	v_pk_mul_f32 v[44:45], v[44:45], v[208:209]
	v_pk_mul_f32 v[46:47], v[46:47], v[210:211]
	v_pk_mul_f32 v[48:49], v[48:49], v[212:213]
	v_pk_mul_f32 v[50:51], v[50:51], v[214:215]
	v_pk_mul_f32 v[20:21], v[20:21], v[200:201]
	v_pk_mul_f32 v[22:23], v[22:23], v[202:203]
	v_pk_mul_f32 v[24:25], v[24:25], v[204:205]
	v_pk_mul_f32 v[26:27], v[26:27], v[206:207]
	v_pk_mul_f32 v[28:29], v[28:29], v[208:209]
	v_pk_mul_f32 v[30:31], v[30:31], v[210:211]
	v_pk_mul_f32 v[32:33], v[32:33], v[212:213]
	v_pk_mul_f32 v[34:35], v[34:35], v[214:215]
	v_pk_mul_f32 v[4:5], v[4:5], v[200:201]
	v_pk_mul_f32 v[6:7], v[6:7], v[202:203]
	v_pk_mul_f32 v[8:9], v[8:9], v[204:205]
	v_pk_mul_f32 v[10:11], v[10:11], v[206:207]
	v_pk_mul_f32 v[12:13], v[12:13], v[208:209]
	v_pk_mul_f32 v[14:15], v[14:15], v[210:211]
	v_pk_mul_f32 v[16:17], v[16:17], v[212:213]
	v_pk_mul_f32 v[18:19], v[18:19], v[214:215]
	v_cvt_pk_fp8_f32 v232, v164, v165
	v_cvt_pk_fp8_f32 v233, v168, v169
	v_cvt_pk_fp8_f32 v234, v172, v173
	v_cvt_pk_fp8_f32 v235, v176, v177
	v_cvt_pk_fp8_f32 v232, v166, v167 op_sel:[0,0,1]
	v_cvt_pk_fp8_f32 v233, v170, v171 op_sel:[0,0,1]
	v_cvt_pk_fp8_f32 v234, v174, v175 op_sel:[0,0,1]
	v_cvt_pk_fp8_f32 v235, v178, v179 op_sel:[0,0,1]
	v_cvt_pk_fp8_f32 v236, v116, v117
	v_cvt_pk_fp8_f32 v237, v120, v121
	v_cvt_pk_fp8_f32 v238, v124, v125
	v_cvt_pk_fp8_f32 v239, v128, v129
	v_cvt_pk_fp8_f32 v236, v118, v119 op_sel:[0,0,1]
	v_cvt_pk_fp8_f32 v237, v122, v123 op_sel:[0,0,1]
	v_cvt_pk_fp8_f32 v238, v126, v127 op_sel:[0,0,1]
	v_cvt_pk_fp8_f32 v239, v130, v131 op_sel:[0,0,1]
	ds_read_b128 v[208:211], v197 offset:10240
	ds_read_b128 v[212:215], v198 offset:10240
	ds_read_b128 v[200:203], v197 offset:8192
	ds_read_b128 v[204:207], v198 offset:8192

.Lring_noload_b1:
	ds_read_b128 v[116:119], v192 offset:32768
	ds_read_b128 v[120:123], v193 offset:32768
	v_mov_b32_e32 v254, v180
	v_mov_b32_e32 v255, v182
	ds_write_b64 v189, v[254:255] offset:16384
	v_mov_b32_e32 v244, v181
	v_mov_b32_e32 v245, v183
	ds_write_b64 v190, v[244:245] offset:16384
	ds_write_b128 v191, v[248:251] offset:49152
	v_exp_f32_e32 v84, v84
	v_exp_f32_e32 v85, v85
	v_exp_f32_e32 v86, v86
	v_exp_f32_e32 v87, v87
	v_exp_f32_e32 v88, v88
	v_exp_f32_e32 v89, v89
	s_waitcnt lgkmcnt(7)
	v_mfma_scale_f32_32x32x64_f8f6f4 v[36:51], v[232:239], v[208:215], v[36:51], v188, v188 op_sel_hi:[0,0,0]
	v_exp_f32_e32 v90, v90
	v_exp_f32_e32 v91, v91
	v_exp_f32_e32 v92, v92
	v_exp_f32_e32 v93, v93
	v_exp_f32_e32 v94, v94
	v_exp_f32_e32 v95, v95
	v_exp_f32_e32 v96, v96
	v_exp_f32_e32 v97, v97
	v_exp_f32_e32 v98, v98
	v_exp_f32_e32 v99, v99
	s_waitcnt lgkmcnt(5)
	v_mfma_scale_f32_32x32x64_f8f6f4 v[52:67], v[232:239], v[200:207], v[52:67], v188, v188 op_sel_hi:[0,0,0]
	ds_read_b128 v[208:211], v197 offset:14336
	ds_read_b128 v[212:215], v198 offset:14336
	ds_read_b128 v[200:203], v197 offset:12288
	ds_read_b128 v[204:207], v198 offset:12288
	v_exp_f32_e32 v68, v68
	v_exp_f32_e32 v69, v69
	v_exp_f32_e32 v70, v70
	v_exp_f32_e32 v71, v71
	v_exp_f32_e32 v72, v72
	v_exp_f32_e32 v73, v73
	v_exp_f32_e32 v74, v74
	v_exp_f32_e32 v75, v75
	v_exp_f32_e32 v76, v76
	v_exp_f32_e32 v77, v77
	s_waitcnt lgkmcnt(2)
	v_mfma_scale_f32_32x32x64_f8f6f4 v[4:19], v[232:239], v[208:215], v[4:19], v188, v188 op_sel_hi:[0,0,0]
	ds_read_b128 v[208:211], v194 offset:32768
	ds_read_b128 v[212:215], v195 offset:32768
	v_exp_f32_e32 v78, v78
	v_exp_f32_e32 v79, v79
	v_exp_f32_e32 v80, v80
	v_exp_f32_e32 v81, v81
	v_exp_f32_e32 v82, v82
	v_exp_f32_e32 v83, v83
	v_add_f32_e32 v240, v84, v85
	v_add_f32_e32 v241, v68, v69
	v_add_f32_e32 v240, v86, v240
	v_add_f32_e32 v241, v70, v241
	s_waitcnt lgkmcnt(2)
	v_mfma_scale_f32_32x32x64_f8f6f4 v[20:35], v[232:239], v[200:207], v[20:35], v188, v188 op_sel_hi:[0,0,0]
	ds_read_b128 v[200:203], v192 offset:36864
	ds_read_b128 v[204:207], v193 offset:36864
	v_add_f32_e32 v240, v87, v240
	v_add_f32_e32 v241, v71, v241
	v_add_f32_e32 v240, v88, v240
	v_add_f32_e32 v241, v72, v241
	v_add_f32_e32 v240, v89, v240
	v_add_f32_e32 v241, v73, v241
	v_add_f32_e32 v240, v90, v240
	v_add_f32_e32 v241, v74, v241
	v_add_f32_e32 v240, v91, v240
	v_add_f32_e32 v241, v75, v241
	v_mfma_scale_f32_32x32x64_f8f6f4 v[164:179], v[116:123], v[100:107], v[216:231], v188, v247 op_sel_hi:[0,0,0]
	v_add_f32_e32 v240, v92, v240
	v_add_f32_e32 v241, v76, v241
	v_add_f32_e32 v240, v93, v240
	v_add_f32_e32 v241, v77, v241
	v_add_f32_e32 v240, v94, v240
	v_add_f32_e32 v241, v78, v241
	v_add_f32_e32 v240, v95, v240
	v_add_f32_e32 v241, v79, v241
	v_add_f32_e32 v240, v96, v240
	v_add_f32_e32 v241, v80, v241
	s_waitcnt lgkmcnt(2)
	v_mfma_scale_f32_32x32x64_f8f6f4 v[164:179], v[208:215], v[108:115], v[164:179], v188, v247 op_sel_hi:[0,0,0]
	ds_read_b128 v[208:211], v197 offset:26624
	ds_read_b128 v[212:215], v198 offset:26624
	v_add_f32_e32 v240, v97, v240
	v_add_f32_e32 v241, v81, v241
	v_add_f32_e32 v240, v98, v240
	v_add_f32_e32 v241, v82, v241
	v_add_f32_e32 v240, v99, v240
	v_add_f32_e32 v241, v83, v241
	v_add_f32_e32 v154, v240, v241
	v_mov_b32_e32 v155, v154
	s_nop 0
	s_nop 0
	v_permlane32_swap_b32_e32 v154, v155
	v_add_f32_e32 v154, v154, v155
	s_waitcnt lgkmcnt(2)
	v_mfma_scale_f32_32x32x64_f8f6f4 v[116:131], v[200:207], v[100:107], v[216:231], v188, v247 op_sel_hi:[0,0,0]
	ds_read_b128 v[200:203], v194 offset:36864
	ds_read_b128 v[204:207], v195 offset:36864
	v_add_f32_e32 v145, v145, v154
	v_cvt_pk_fp8_f32 v232, v84, v85
	v_cvt_pk_fp8_f32 v233, v88, v89
	v_cvt_pk_fp8_f32 v234, v92, v93
	v_cvt_pk_fp8_f32 v235, v96, v97
	v_cvt_pk_fp8_f32 v232, v86, v87 op_sel:[0,0,1]
	v_cvt_pk_fp8_f32 v233, v90, v91 op_sel:[0,0,1]
	v_cvt_pk_fp8_f32 v234, v94, v95 op_sel:[0,0,1]
	v_cvt_pk_fp8_f32 v235, v98, v99 op_sel:[0,0,1]
	v_cvt_pk_fp8_f32 v236, v68, v69
	s_waitcnt lgkmcnt(0)
	v_mfma_scale_f32_32x32x64_f8f6f4 v[116:131], v[200:207], v[108:115], v[116:131], v188, v247 op_sel_hi:[0,0,0]
	ds_read_b128 v[200:203], v197 offset:24576
	ds_read_b128 v[204:207], v198 offset:24576
	v_cvt_pk_fp8_f32 v237, v72, v73
	v_cvt_pk_fp8_f32 v238, v76, v77
	v_cvt_pk_fp8_f32 v239, v80, v81
	v_cvt_pk_fp8_f32 v236, v70, v71 op_sel:[0,0,1]
	v_cvt_pk_fp8_f32 v237, v74, v75 op_sel:[0,0,1]
	v_cvt_pk_fp8_f32 v238, v78, v79 op_sel:[0,0,1]
	v_cvt_pk_fp8_f32 v239, v82, v83 op_sel:[0,0,1]
	v_cmp_ge_f32_e32 vcc, 0x43c80000, v154
	s_cmp_eq_u64 vcc, exec
	s_cbranch_scc1 .Lring_norare_b1
	s_nop 15
	s_nop 15
	v_max3_f32 v240, v84, v85, v86
	v_max3_f32 v240, v240, v87, v88
	v_max3_f32 v240, v240, v89, v90
	v_max3_f32 v240, v240, v91, v92
	v_max3_f32 v240, v240, v93, v94
	v_max3_f32 v240, v240, v95, v96
	v_max3_f32 v240, v240, v97, v98
	v_max3_f32 v240, v240, v99, v68
	v_max3_f32 v240, v240, v69, v70
	v_max3_f32 v240, v240, v71, v72
	v_max3_f32 v240, v240, v73, v74
	v_max3_f32 v240, v240, v75, v76
	v_max3_f32 v240, v240, v77, v78
	v_max3_f32 v240, v240, v79, v80
	v_max3_f32 v240, v240, v81, v82
	v_max_f32_e32 v240, v240, v83
	v_mov_b32_e32 v241, v240
	s_nop 1
	v_permlane32_swap_b32_e32 v240, v241
	v_max_f32_e32 v240, v240, v241
	v_log_f32_e32 v2, v240
	s_nop 0
	v_ceil_f32_e32 v2, v2
	v_max_f32_e32 v2, 0, v2
	v_exp_f32_e64 v147, -v2
	s_nop 0
	v_fmamk_f32 v153, v2, 0x41000000, v153
	v_mul_f32_e32 v84, v84, v147
	v_mul_f32_e32 v85, v85, v147
	v_mul_f32_e32 v86, v86, v147
	v_mul_f32_e32 v87, v87, v147
	v_mul_f32_e32 v88, v88, v147
	v_mul_f32_e32 v89, v89, v147
	v_mul_f32_e32 v90, v90, v147
	v_mul_f32_e32 v91, v91, v147
	v_mul_f32_e32 v92, v92, v147
	v_mul_f32_e32 v93, v93, v147
	v_mul_f32_e32 v94, v94, v147
	v_mul_f32_e32 v95, v95, v147
	v_mul_f32_e32 v96, v96, v147
	v_mul_f32_e32 v97, v97, v147
	v_mul_f32_e32 v98, v98, v147
	v_mul_f32_e32 v99, v99, v147
	v_mul_f32_e32 v68, v68, v147
	v_mul_f32_e32 v69, v69, v147
	v_mul_f32_e32 v70, v70, v147
	v_mul_f32_e32 v71, v71, v147
	v_mul_f32_e32 v72, v72, v147
	v_mul_f32_e32 v73, v73, v147
	v_mul_f32_e32 v74, v74, v147
	v_mul_f32_e32 v75, v75, v147
	v_mul_f32_e32 v76, v76, v147
	v_mul_f32_e32 v77, v77, v147
	v_mul_f32_e32 v78, v78, v147
	v_mul_f32_e32 v79, v79, v147
	v_mul_f32_e32 v80, v80, v147
	v_mul_f32_e32 v81, v81, v147
	v_mul_f32_e32 v82, v82, v147
	v_mul_f32_e32 v83, v83, v147
	v_mul_f32_e32 v145, v145, v147
	v_sub_f32_e32 v164, v164, v2
	v_sub_f32_e32 v165, v165, v2
	v_sub_f32_e32 v166, v166, v2
	v_sub_f32_e32 v167, v167, v2
	v_sub_f32_e32 v168, v168, v2
	v_sub_f32_e32 v169, v169, v2
	v_sub_f32_e32 v170, v170, v2
	v_sub_f32_e32 v171, v171, v2
	v_sub_f32_e32 v172, v172, v2
	v_sub_f32_e32 v173, v173, v2
	v_sub_f32_e32 v174, v174, v2
	v_sub_f32_e32 v175, v175, v2
	v_sub_f32_e32 v176, v176, v2
	v_sub_f32_e32 v177, v177, v2
	v_sub_f32_e32 v178, v178, v2
	v_sub_f32_e32 v179, v179, v2
	v_sub_f32_e32 v116, v116, v2
	v_sub_f32_e32 v117, v117, v2
	v_sub_f32_e32 v118, v118, v2
	v_sub_f32_e32 v119, v119, v2
	v_sub_f32_e32 v120, v120, v2
	v_sub_f32_e32 v121, v121, v2
	v_sub_f32_e32 v122, v122, v2
	v_sub_f32_e32 v123, v123, v2
	v_sub_f32_e32 v124, v124, v2
	v_sub_f32_e32 v125, v125, v2
	v_sub_f32_e32 v126, v126, v2
	v_sub_f32_e32 v127, v127, v2
	v_sub_f32_e32 v128, v128, v2
	v_sub_f32_e32 v129, v129, v2
	v_sub_f32_e32 v130, v130, v2
	v_sub_f32_e32 v131, v131, v2
	v_sub_f32_e32 v216, v216, v2
	v_sub_f32_e32 v217, v217, v2
	v_sub_f32_e32 v218, v218, v2
	v_sub_f32_e32 v219, v219, v2
	v_sub_f32_e32 v220, v220, v2
	v_sub_f32_e32 v221, v221, v2
	v_sub_f32_e32 v222, v222, v2
	v_sub_f32_e32 v223, v223, v2
	v_sub_f32_e32 v224, v224, v2
	v_sub_f32_e32 v225, v225, v2
	v_sub_f32_e32 v226, v226, v2
	v_sub_f32_e32 v227, v227, v2
	v_sub_f32_e32 v228, v228, v2
	v_sub_f32_e32 v229, v229, v2
	v_sub_f32_e32 v230, v230, v2
	v_sub_f32_e32 v231, v231, v2
	s_and_saveexec_b64 s[10:11], s[6:7]
	ds_write_b32 v184, v147 offset:128
	s_or_b64 exec, exec, s[10:11]
	s_waitcnt lgkmcnt(0)
	v_add_u32_e32 v253, v135, v185
	ds_read_b128 v[212:215], v253 offset:224
	ds_read_b128 v[208:211], v253 offset:192
	ds_read_b128 v[204:207], v253 offset:160
	ds_read_b128 v[200:203], v253 offset:128
	s_waitcnt lgkmcnt(0)
	v_pk_mul_f32 v[52:53], v[52:53], v[200:201]
	v_pk_mul_f32 v[54:55], v[54:55], v[202:203]
	v_pk_mul_f32 v[56:57], v[56:57], v[204:205]
	v_pk_mul_f32 v[58:59], v[58:59], v[206:207]
	v_pk_mul_f32 v[60:61], v[60:61], v[208:209]
	v_pk_mul_f32 v[62:63], v[62:63], v[210:211]
	v_pk_mul_f32 v[64:65], v[64:65], v[212:213]
	v_pk_mul_f32 v[66:67], v[66:67], v[214:215]
	v_pk_mul_f32 v[36:37], v[36:37], v[200:201]
	v_pk_mul_f32 v[38:39], v[38:39], v[202:203]
	v_pk_mul_f32 v[40:41], v[40:41], v[204:205]
	v_pk_mul_f32 v[42:43], v[42:43], v[206:207]
	v_pk_mul_f32 v[44:45], v[44:45], v[208:209]
	v_pk_mul_f32 v[46:47], v[46:47], v[210:211]
	v_pk_mul_f32 v[48:49], v[48:49], v[212:213]
	v_pk_mul_f32 v[50:51], v[50:51], v[214:215]
	v_pk_mul_f32 v[20:21], v[20:21], v[200:201]
	v_pk_mul_f32 v[22:23], v[22:23], v[202:203]
	v_pk_mul_f32 v[24:25], v[24:25], v[204:205]
	v_pk_mul_f32 v[26:27], v[26:27], v[206:207]
	v_pk_mul_f32 v[28:29], v[28:29], v[208:209]
	v_pk_mul_f32 v[30:31], v[30:31], v[210:211]
	v_pk_mul_f32 v[32:33], v[32:33], v[212:213]
	v_pk_mul_f32 v[34:35], v[34:35], v[214:215]
	v_pk_mul_f32 v[4:5], v[4:5], v[200:201]
	v_pk_mul_f32 v[6:7], v[6:7], v[202:203]
	v_pk_mul_f32 v[8:9], v[8:9], v[204:205]
	v_pk_mul_f32 v[10:11], v[10:11], v[206:207]
	v_pk_mul_f32 v[12:13], v[12:13], v[208:209]
	v_pk_mul_f32 v[14:15], v[14:15], v[210:211]
	v_pk_mul_f32 v[16:17], v[16:17], v[212:213]
	v_pk_mul_f32 v[18:19], v[18:19], v[214:215]
	v_cvt_pk_fp8_f32 v232, v84, v85
	v_cvt_pk_fp8_f32 v233, v88, v89
	v_cvt_pk_fp8_f32 v234, v92, v93
	v_cvt_pk_fp8_f32 v235, v96, v97
	v_cvt_pk_fp8_f32 v232, v86, v87 op_sel:[0,0,1]
	v_cvt_pk_fp8_f32 v233, v90, v91 op_sel:[0,0,1]
	v_cvt_pk_fp8_f32 v234, v94, v95 op_sel:[0,0,1]
	v_cvt_pk_fp8_f32 v235, v98, v99 op_sel:[0,0,1]
	v_cvt_pk_fp8_f32 v236, v68, v69
	v_cvt_pk_fp8_f32 v237, v72, v73
	v_cvt_pk_fp8_f32 v238, v76, v77
	v_cvt_pk_fp8_f32 v239, v80, v81
	v_cvt_pk_fp8_f32 v236, v70, v71 op_sel:[0,0,1]
	v_cvt_pk_fp8_f32 v237, v74, v75 op_sel:[0,0,1]
	v_cvt_pk_fp8_f32 v238, v78, v79 op_sel:[0,0,1]
	v_cvt_pk_fp8_f32 v239, v82, v83 op_sel:[0,0,1]
	ds_read_b128 v[208:211], v197 offset:26624
	ds_read_b128 v[212:215], v198 offset:26624
	ds_read_b128 v[200:203], v197 offset:24576
	ds_read_b128 v[204:207], v198 offset:24576
.Lring_norare_b1:
	s_add_i32 s15, s15, 2
	v_lshl_add_u64 v[150:151], v[150:151], 0, s[28:29]
	v_add_u32_e32 v152, 0x4000, v152
	s_and_b64 vcc, exec, s[8:9]
	s_waitcnt lgkmcnt(4)
	s_barrier
	s_cbranch_vccnz .Lring_drain_b1
	s_branch .LBB0_409
.Lring_drain_b0:
	v_exp_f32_e32 v84, v164
	v_exp_f32_e32 v85, v165
	v_exp_f32_e32 v86, v166
	v_exp_f32_e32 v87, v167
	v_exp_f32_e32 v88, v168
	v_exp_f32_e32 v89, v169
	v_exp_f32_e32 v90, v170
	v_exp_f32_e32 v91, v171
	v_exp_f32_e32 v92, v172
	v_exp_f32_e32 v93, v173
	v_exp_f32_e32 v94, v174
	v_exp_f32_e32 v95, v175
	v_exp_f32_e32 v96, v176
	s_waitcnt lgkmcnt(2)
	v_mfma_scale_f32_32x32x64_f8f6f4 v[36:51], v[232:239], v[208:215], v[36:51], v188, v188 op_sel_hi:[0,0,0]
	v_exp_f32_e32 v97, v177
	v_exp_f32_e32 v98, v178
	v_exp_f32_e32 v99, v179
	v_exp_f32_e32 v68, v116
	v_exp_f32_e32 v69, v117
	v_exp_f32_e32 v70, v118
	v_exp_f32_e32 v71, v119
	v_exp_f32_e32 v72, v120
	v_exp_f32_e32 v73, v121
	v_exp_f32_e32 v74, v122
	v_exp_f32_e32 v75, v123
	v_exp_f32_e32 v76, v124
	v_exp_f32_e32 v77, v125
	v_exp_f32_e32 v78, v126
	s_waitcnt lgkmcnt(0)
	v_mfma_scale_f32_32x32x64_f8f6f4 v[52:67], v[232:239], v[200:207], v[52:67], v188, v188 op_sel_hi:[0,0,0]
	ds_read_b128 v[208:211], v197 offset:22528
	ds_read_b128 v[212:215], v198 offset:22528
	ds_read_b128 v[200:203], v197 offset:20480
	ds_read_b128 v[204:207], v198 offset:20480
	v_exp_f32_e32 v79, v127
	v_exp_f32_e32 v80, v128
	v_exp_f32_e32 v81, v129
	v_exp_f32_e32 v82, v130
	v_exp_f32_e32 v83, v131
	v_add_f32_e32 v240, v84, v85
	v_add_f32_e32 v241, v68, v69
	v_add_f32_e32 v240, v86, v240
	v_add_f32_e32 v241, v70, v241
	v_add_f32_e32 v240, v87, v240
	v_add_f32_e32 v241, v71, v241
	v_add_f32_e32 v240, v88, v240
	v_add_f32_e32 v241, v72, v241
	v_add_f32_e32 v240, v89, v240
	s_waitcnt lgkmcnt(2)
	v_mfma_scale_f32_32x32x64_f8f6f4 v[4:19], v[232:239], v[208:215], v[4:19], v188, v188 op_sel_hi:[0,0,0]
	v_add_f32_e32 v241, v73, v241
	v_add_f32_e32 v240, v90, v240
	v_add_f32_e32 v241, v74, v241
	v_add_f32_e32 v240, v91, v240
	v_add_f32_e32 v241, v75, v241
	v_add_f32_e32 v240, v92, v240
	v_add_f32_e32 v241, v76, v241
	v_add_f32_e32 v240, v93, v240
	v_add_f32_e32 v241, v77, v241
	v_add_f32_e32 v240, v94, v240
	v_add_f32_e32 v241, v78, v241
	v_add_f32_e32 v240, v95, v240
	v_add_f32_e32 v241, v79, v241
	v_add_f32_e32 v240, v96, v240
	s_waitcnt lgkmcnt(0)
	v_mfma_scale_f32_32x32x64_f8f6f4 v[20:35], v[232:239], v[200:207], v[20:35], v188, v188 op_sel_hi:[0,0,0]
	v_add_f32_e32 v241, v80, v241
	v_add_f32_e32 v240, v97, v240
	v_add_f32_e32 v241, v81, v241
	v_add_f32_e32 v240, v98, v240
	v_add_f32_e32 v241, v82, v241
	v_add_f32_e32 v240, v99, v240
	v_add_f32_e32 v241, v83, v241
	v_add_f32_e32 v154, v240, v241
	v_mov_b32_e32 v155, v154
	s_nop 0
	s_nop 0
	v_permlane32_swap_b32_e32 v154, v155
	v_add_f32_e32 v154, v154, v155
	v_cmp_ge_f32_e32 vcc, 0x43c80000, v154
	s_cmp_eq_u64 vcc, exec
	s_cbranch_scc1 .Lring_nodr_b0
	s_nop 15
	s_nop 15
	v_max3_f32 v240, v84, v85, v86
	v_max3_f32 v240, v240, v87, v88
	v_max3_f32 v240, v240, v89, v90
	v_max3_f32 v240, v240, v91, v92
	v_max3_f32 v240, v240, v93, v94
	v_max3_f32 v240, v240, v95, v96
	v_max3_f32 v240, v240, v97, v98
	v_max3_f32 v240, v240, v99, v68
	v_max3_f32 v240, v240, v69, v70
	v_max3_f32 v240, v240, v71, v72
	v_max3_f32 v240, v240, v73, v74
	v_max3_f32 v240, v240, v75, v76
	v_max3_f32 v240, v240, v77, v78
	v_max3_f32 v240, v240, v79, v80
	v_max3_f32 v240, v240, v81, v82
	v_max_f32_e32 v240, v240, v83
	v_mov_b32_e32 v241, v240
	s_nop 1
	v_permlane32_swap_b32_e32 v240, v241
	v_max_f32_e32 v240, v240, v241
	v_log_f32_e32 v2, v240
	s_nop 0
	v_ceil_f32_e32 v2, v2
	v_max_f32_e32 v2, 0, v2
	v_exp_f32_e64 v147, -v2
	s_nop 0
	v_fmamk_f32 v153, v2, 0x41000000, v153
	v_mul_f32_e32 v84, v84, v147
	v_mul_f32_e32 v85, v85, v147
	v_mul_f32_e32 v86, v86, v147
	v_mul_f32_e32 v87, v87, v147
	v_mul_f32_e32 v88, v88, v147
	v_mul_f32_e32 v89, v89, v147
	v_mul_f32_e32 v90, v90, v147
	v_mul_f32_e32 v91, v91, v147
	v_mul_f32_e32 v92, v92, v147
	v_mul_f32_e32 v93, v93, v147
	v_mul_f32_e32 v94, v94, v147
	v_mul_f32_e32 v95, v95, v147
	v_mul_f32_e32 v96, v96, v147
	v_mul_f32_e32 v97, v97, v147
	v_mul_f32_e32 v98, v98, v147
	v_mul_f32_e32 v99, v99, v147
	v_mul_f32_e32 v68, v68, v147
	v_mul_f32_e32 v69, v69, v147
	v_mul_f32_e32 v70, v70, v147
	v_mul_f32_e32 v71, v71, v147
	v_mul_f32_e32 v72, v72, v147
	v_mul_f32_e32 v73, v73, v147
	v_mul_f32_e32 v74, v74, v147
	v_mul_f32_e32 v75, v75, v147
	v_mul_f32_e32 v76, v76, v147
	v_mul_f32_e32 v77, v77, v147
	v_mul_f32_e32 v78, v78, v147
	v_mul_f32_e32 v79, v79, v147
	v_mul_f32_e32 v80, v80, v147
	v_mul_f32_e32 v81, v81, v147
	v_mul_f32_e32 v82, v82, v147
	v_mul_f32_e32 v83, v83, v147
	v_mul_f32_e32 v145, v145, v147
	s_and_saveexec_b64 s[10:11], s[6:7]
	ds_write_b32 v184, v147 offset:128
	s_or_b64 exec, exec, s[10:11]
	s_waitcnt lgkmcnt(0)
	v_add_u32_e32 v253, v135, v185
	ds_read_b128 v[212:215], v253 offset:224
	ds_read_b128 v[208:211], v253 offset:192
	ds_read_b128 v[204:207], v253 offset:160
	ds_read_b128 v[200:203], v253 offset:128
	s_waitcnt lgkmcnt(0)
	v_pk_mul_f32 v[52:53], v[52:53], v[200:201]
	v_pk_mul_f32 v[54:55], v[54:55], v[202:203]
	v_pk_mul_f32 v[56:57], v[56:57], v[204:205]
	v_pk_mul_f32 v[58:59], v[58:59], v[206:207]
	v_pk_mul_f32 v[60:61], v[60:61], v[208:209]
	v_pk_mul_f32 v[62:63], v[62:63], v[210:211]
	v_pk_mul_f32 v[64:65], v[64:65], v[212:213]
	v_pk_mul_f32 v[66:67], v[66:67], v[214:215]
	v_pk_mul_f32 v[36:37], v[36:37], v[200:201]
	v_pk_mul_f32 v[38:39], v[38:39], v[202:203]
	v_pk_mul_f32 v[40:41], v[40:41], v[204:205]
	v_pk_mul_f32 v[42:43], v[42:43], v[206:207]
	v_pk_mul_f32 v[44:45], v[44:45], v[208:209]
	v_pk_mul_f32 v[46:47], v[46:47], v[210:211]
	v_pk_mul_f32 v[48:49], v[48:49], v[212:213]
	v_pk_mul_f32 v[50:51], v[50:51], v[214:215]
	v_pk_mul_f32 v[20:21], v[20:21], v[200:201]
	v_pk_mul_f32 v[22:23], v[22:23], v[202:203]
	v_pk_mul_f32 v[24:25], v[24:25], v[204:205]
	v_pk_mul_f32 v[26:27], v[26:27], v[206:207]
	v_pk_mul_f32 v[28:29], v[28:29], v[208:209]
	v_pk_mul_f32 v[30:31], v[30:31], v[210:211]
	v_pk_mul_f32 v[32:33], v[32:33], v[212:213]
	v_pk_mul_f32 v[34:35], v[34:35], v[214:215]
	v_pk_mul_f32 v[4:5], v[4:5], v[200:201]
	v_pk_mul_f32 v[6:7], v[6:7], v[202:203]
	v_pk_mul_f32 v[8:9], v[8:9], v[204:205]
	v_pk_mul_f32 v[10:11], v[10:11], v[206:207]
	v_pk_mul_f32 v[12:13], v[12:13], v[208:209]
	v_pk_mul_f32 v[14:15], v[14:15], v[210:211]
	v_pk_mul_f32 v[16:17], v[16:17], v[212:213]
	v_pk_mul_f32 v[18:19], v[18:19], v[214:215]
.Lring_nodr_b0:
	s_nop 1
	v_mov_b32_e32 v173, v84
	v_mov_b32_e32 v177, v85
	v_mov_b32_e32 v165, v86
	v_mov_b32_e32 v166, v87
	v_mov_b32_e32 v174, v88
	v_mov_b32_e32 v178, v89
	v_mov_b32_e32 v167, v90
	v_mov_b32_e32 v168, v91
	v_mov_b32_e32 v175, v92
	v_mov_b32_e32 v179, v93
	v_mov_b32_e32 v169, v94
	v_mov_b32_e32 v170, v95
	v_mov_b32_e32 v176, v96
	v_mov_b32_e32 v180, v97
	v_mov_b32_e32 v171, v98
	v_mov_b32_e32 v172, v99
	v_mov_b32_e32 v154, v68
	v_mov_b32_e32 v155, v69
	v_mov_b32_e32 v130, v70
	v_mov_b32_e32 v131, v71
	v_mov_b32_e32 v128, v72
	v_mov_b32_e32 v129, v73
	v_mov_b32_e32 v126, v74
	v_mov_b32_e32 v127, v75
	v_mov_b32_e32 v124, v76
	v_mov_b32_e32 v125, v77
	v_mov_b32_e32 v160, v78
	v_mov_b32_e32 v161, v79
	v_mov_b32_e32 v158, v80
	v_mov_b32_e32 v159, v81
	v_mov_b32_e32 v156, v82
	v_mov_b32_e32 v157, v83
	s_branch .LBB0_421
.Lring_drain_b1:
	v_exp_f32_e32 v84, v164
	v_exp_f32_e32 v85, v165
	v_exp_f32_e32 v86, v166
	v_exp_f32_e32 v87, v167
	v_exp_f32_e32 v88, v168
	v_exp_f32_e32 v89, v169
	v_exp_f32_e32 v90, v170
	v_exp_f32_e32 v91, v171
	v_exp_f32_e32 v92, v172
	v_exp_f32_e32 v93, v173
	v_exp_f32_e32 v94, v174
	v_exp_f32_e32 v95, v175
	v_exp_f32_e32 v96, v176
	s_waitcnt lgkmcnt(2)
	v_mfma_scale_f32_32x32x64_f8f6f4 v[36:51], v[232:239], v[208:215], v[36:51], v188, v188 op_sel_hi:[0,0,0]
	v_exp_f32_e32 v97, v177
	v_exp_f32_e32 v98, v178
	v_exp_f32_e32 v99, v179
	v_exp_f32_e32 v68, v116
	v_exp_f32_e32 v69, v117
	v_exp_f32_e32 v70, v118
	v_exp_f32_e32 v71, v119
	v_exp_f32_e32 v72, v120
	v_exp_f32_e32 v73, v121
	v_exp_f32_e32 v74, v122
	v_exp_f32_e32 v75, v123
	v_exp_f32_e32 v76, v124
	v_exp_f32_e32 v77, v125
	v_exp_f32_e32 v78, v126
	s_waitcnt lgkmcnt(0)
	v_mfma_scale_f32_32x32x64_f8f6f4 v[52:67], v[232:239], v[200:207], v[52:67], v188, v188 op_sel_hi:[0,0,0]
	ds_read_b128 v[208:211], v197 offset:30720
	ds_read_b128 v[212:215], v198 offset:30720
	ds_read_b128 v[200:203], v197 offset:28672
	ds_read_b128 v[204:207], v198 offset:28672
	v_exp_f32_e32 v79, v127
	v_exp_f32_e32 v80, v128
	v_exp_f32_e32 v81, v129
	v_exp_f32_e32 v82, v130
	v_exp_f32_e32 v83, v131
	v_add_f32_e32 v240, v84, v85
	v_add_f32_e32 v241, v68, v69
	v_add_f32_e32 v240, v86, v240
	v_add_f32_e32 v241, v70, v241
	v_add_f32_e32 v240, v87, v240
	v_add_f32_e32 v241, v71, v241
	v_add_f32_e32 v240, v88, v240
	v_add_f32_e32 v241, v72, v241
	v_add_f32_e32 v240, v89, v240
	s_waitcnt lgkmcnt(2)
	v_mfma_scale_f32_32x32x64_f8f6f4 v[4:19], v[232:239], v[208:215], v[4:19], v188, v188 op_sel_hi:[0,0,0]
	v_add_f32_e32 v241, v73, v241
	v_add_f32_e32 v240, v90, v240
	v_add_f32_e32 v241, v74, v241
	v_add_f32_e32 v240, v91, v240
	v_add_f32_e32 v241, v75, v241
	v_add_f32_e32 v240, v92, v240
	v_add_f32_e32 v241, v76, v241
	v_add_f32_e32 v240, v93, v240
	v_add_f32_e32 v241, v77, v241
	v_add_f32_e32 v240, v94, v240
	v_add_f32_e32 v241, v78, v241
	v_add_f32_e32 v240, v95, v240
	v_add_f32_e32 v241, v79, v241
	v_add_f32_e32 v240, v96, v240
	s_waitcnt lgkmcnt(0)
	v_mfma_scale_f32_32x32x64_f8f6f4 v[20:35], v[232:239], v[200:207], v[20:35], v188, v188 op_sel_hi:[0,0,0]
	v_add_f32_e32 v241, v80, v241
	v_add_f32_e32 v240, v97, v240
	v_add_f32_e32 v241, v81, v241
	v_add_f32_e32 v240, v98, v240
	v_add_f32_e32 v241, v82, v241
	v_add_f32_e32 v240, v99, v240
	v_add_f32_e32 v241, v83, v241
	v_add_f32_e32 v154, v240, v241
	v_mov_b32_e32 v155, v154
	s_nop 0
	s_nop 0
	v_permlane32_swap_b32_e32 v154, v155
	v_add_f32_e32 v154, v154, v155
	v_cmp_ge_f32_e32 vcc, 0x43c80000, v154
	s_cmp_eq_u64 vcc, exec
	s_cbranch_scc1 .Lring_nodr_b1
	s_nop 15
	s_nop 15
	v_max3_f32 v240, v84, v85, v86
	v_max3_f32 v240, v240, v87, v88
	v_max3_f32 v240, v240, v89, v90
	v_max3_f32 v240, v240, v91, v92
	v_max3_f32 v240, v240, v93, v94
	v_max3_f32 v240, v240, v95, v96
	v_max3_f32 v240, v240, v97, v98
	v_max3_f32 v240, v240, v99, v68
	v_max3_f32 v240, v240, v69, v70
	v_max3_f32 v240, v240, v71, v72
	v_max3_f32 v240, v240, v73, v74
	v_max3_f32 v240, v240, v75, v76
	v_max3_f32 v240, v240, v77, v78
	v_max3_f32 v240, v240, v79, v80
	v_max3_f32 v240, v240, v81, v82
	v_max_f32_e32 v240, v240, v83
	v_mov_b32_e32 v241, v240
	s_nop 1
	v_permlane32_swap_b32_e32 v240, v241
	v_max_f32_e32 v240, v240, v241
	v_log_f32_e32 v2, v240
	s_nop 0
	v_ceil_f32_e32 v2, v2
	v_max_f32_e32 v2, 0, v2
	v_exp_f32_e64 v147, -v2
	s_nop 0
	v_fmamk_f32 v153, v2, 0x41000000, v153
	v_mul_f32_e32 v84, v84, v147
	v_mul_f32_e32 v85, v85, v147
	v_mul_f32_e32 v86, v86, v147
	v_mul_f32_e32 v87, v87, v147
	v_mul_f32_e32 v88, v88, v147
	v_mul_f32_e32 v89, v89, v147
	v_mul_f32_e32 v90, v90, v147
	v_mul_f32_e32 v91, v91, v147
	v_mul_f32_e32 v92, v92, v147
	v_mul_f32_e32 v93, v93, v147
	v_mul_f32_e32 v94, v94, v147
	v_mul_f32_e32 v95, v95, v147
	v_mul_f32_e32 v96, v96, v147
	v_mul_f32_e32 v97, v97, v147
	v_mul_f32_e32 v98, v98, v147
	v_mul_f32_e32 v99, v99, v147
	v_mul_f32_e32 v68, v68, v147
	v_mul_f32_e32 v69, v69, v147
	v_mul_f32_e32 v70, v70, v147
	v_mul_f32_e32 v71, v71, v147
	v_mul_f32_e32 v72, v72, v147
	v_mul_f32_e32 v73, v73, v147
	v_mul_f32_e32 v74, v74, v147
	v_mul_f32_e32 v75, v75, v147
	v_mul_f32_e32 v76, v76, v147
	v_mul_f32_e32 v77, v77, v147
	v_mul_f32_e32 v78, v78, v147
	v_mul_f32_e32 v79, v79, v147
	v_mul_f32_e32 v80, v80, v147
	v_mul_f32_e32 v81, v81, v147
	v_mul_f32_e32 v82, v82, v147
	v_mul_f32_e32 v83, v83, v147
	v_mul_f32_e32 v145, v145, v147
	s_and_saveexec_b64 s[10:11], s[6:7]
	ds_write_b32 v184, v147 offset:128
	s_or_b64 exec, exec, s[10:11]
	s_waitcnt lgkmcnt(0)
	v_add_u32_e32 v253, v135, v185
	ds_read_b128 v[212:215], v253 offset:224
	ds_read_b128 v[208:211], v253 offset:192
	ds_read_b128 v[204:207], v253 offset:160
	ds_read_b128 v[200:203], v253 offset:128
	s_waitcnt lgkmcnt(0)
	v_pk_mul_f32 v[52:53], v[52:53], v[200:201]
	v_pk_mul_f32 v[54:55], v[54:55], v[202:203]
	v_pk_mul_f32 v[56:57], v[56:57], v[204:205]
	v_pk_mul_f32 v[58:59], v[58:59], v[206:207]
	v_pk_mul_f32 v[60:61], v[60:61], v[208:209]
	v_pk_mul_f32 v[62:63], v[62:63], v[210:211]
	v_pk_mul_f32 v[64:65], v[64:65], v[212:213]
	v_pk_mul_f32 v[66:67], v[66:67], v[214:215]
	v_pk_mul_f32 v[36:37], v[36:37], v[200:201]
	v_pk_mul_f32 v[38:39], v[38:39], v[202:203]
	v_pk_mul_f32 v[40:41], v[40:41], v[204:205]
	v_pk_mul_f32 v[42:43], v[42:43], v[206:207]
	v_pk_mul_f32 v[44:45], v[44:45], v[208:209]
	v_pk_mul_f32 v[46:47], v[46:47], v[210:211]
	v_pk_mul_f32 v[48:49], v[48:49], v[212:213]
	v_pk_mul_f32 v[50:51], v[50:51], v[214:215]
	v_pk_mul_f32 v[20:21], v[20:21], v[200:201]
	v_pk_mul_f32 v[22:23], v[22:23], v[202:203]
	v_pk_mul_f32 v[24:25], v[24:25], v[204:205]
	v_pk_mul_f32 v[26:27], v[26:27], v[206:207]
	v_pk_mul_f32 v[28:29], v[28:29], v[208:209]
	v_pk_mul_f32 v[30:31], v[30:31], v[210:211]
	v_pk_mul_f32 v[32:33], v[32:33], v[212:213]
	v_pk_mul_f32 v[34:35], v[34:35], v[214:215]
	v_pk_mul_f32 v[4:5], v[4:5], v[200:201]
	v_pk_mul_f32 v[6:7], v[6:7], v[202:203]
	v_pk_mul_f32 v[8:9], v[8:9], v[204:205]
	v_pk_mul_f32 v[10:11], v[10:11], v[206:207]
	v_pk_mul_f32 v[12:13], v[12:13], v[208:209]
	v_pk_mul_f32 v[14:15], v[14:15], v[210:211]
	v_pk_mul_f32 v[16:17], v[16:17], v[212:213]
	v_pk_mul_f32 v[18:19], v[18:19], v[214:215]
.Lring_nodr_b1:
	s_nop 1
	v_mov_b32_e32 v173, v84
	v_mov_b32_e32 v177, v85
	v_mov_b32_e32 v165, v86
	v_mov_b32_e32 v166, v87
	v_mov_b32_e32 v174, v88
	v_mov_b32_e32 v178, v89
	v_mov_b32_e32 v167, v90
	v_mov_b32_e32 v168, v91
	v_mov_b32_e32 v175, v92
	v_mov_b32_e32 v179, v93
	v_mov_b32_e32 v169, v94
	v_mov_b32_e32 v170, v95
	v_mov_b32_e32 v176, v96
	v_mov_b32_e32 v180, v97
	v_mov_b32_e32 v171, v98
	v_mov_b32_e32 v172, v99
	v_mov_b32_e32 v154, v68
	v_mov_b32_e32 v155, v69
	v_mov_b32_e32 v130, v70
	v_mov_b32_e32 v131, v71
	v_mov_b32_e32 v128, v72
	v_mov_b32_e32 v129, v73
	v_mov_b32_e32 v126, v74
	v_mov_b32_e32 v127, v75
	v_mov_b32_e32 v124, v76
	v_mov_b32_e32 v125, v77
	v_mov_b32_e32 v160, v78
	v_mov_b32_e32 v161, v79
	v_mov_b32_e32 v158, v80
	v_mov_b32_e32 v159, v81
	v_mov_b32_e32 v156, v82
	v_mov_b32_e32 v157, v83
